# grid barrier rewritten: per-XCD arrival counter, last arriver of each XCD stores a generation flag, all workgroups poll the 8 flags (one atomic round trip fewer)
# baseline (speedup 1.0000x reference)
; __device__ __forceinline__ unsigned xb_ld(unsigned* p)              { return __hip_atomic_load(p, __ATOMIC_RELAXED, __HIP_MEMORY_SCOPE_AGENT); }
; __device__ __forceinline__ unsigned xb_add(unsigned* p, unsigned v) { return __hip_atomic_fetch_add(p, v, __ATOMIC_RELAXED, __HIP_MEMORY_SCOPE_AGENT); }
; #define XB_SPIN(cond, bar) do { unsigned _sp = 0; while (cond) { __builtin_amdgcn_s_sleep(1); \
;     if ((++_sp & 255u) == 0u) { if (xb_ld(&(bar)[XB_TMO])) break; if (_sp > XB_SPIN_CAP) { atomicAdd(&(bar)[XB_TMO], 1u); break; } } } } while (0)
; __device__ __forceinline__ void xcd_barrier(const XcdBarrier& b, const int wave) {
;     asm volatile("s_waitcnt vmcnt(0)" ::: "memory");
;     __syncthreads();
;     if (phase_tid(wave) == 0) {
;         unsigned* bar = b.bar;
;         __builtin_amdgcn_s_waitcnt(0);
;         unsigned nloc = b.st[0], nx = b.st[1];
;         if (nloc == 0u) { xcd_barrier_complete(bar, b.x, nloc, nx); b.st[0] = nloc; b.st[1] = nx; }
;         const unsigned old = xb_add(&bar[XB_XSUB(b.x)], 1u);
;         const unsigned gen = old / nloc;
;         if (old + 1u == (gen + 1u) * nloc) {
;             __builtin_amdgcn_fence(__ATOMIC_RELEASE, "agent");
;             asm volatile("s_waitcnt vmcnt(0)" ::: "memory");
;             const unsigned og = xb_add(&bar[XB_TOP], 1u);
;             const unsigned tg = og / nx;
;             if (og + 1u == (tg + 1u) * nx) xb_add(&bar[XB_TOPGEN], 1u);
;             else XB_SPIN(xb_ld(&bar[XB_TOPGEN]) == tg, bar);
;             __builtin_amdgcn_fence(__ATOMIC_ACQUIRE, "agent");
;             xb_add(&bar[XB_XGEN(b.x)], 1u);
;             asm volatile("s_waitcnt vmcnt(0)" ::: "memory");
;         } else {
;             XB_SPIN(xb_ld(&bar[XB_XGEN(b.x)]) == gen, bar);
;             __builtin_amdgcn_fence(__ATOMIC_ACQUIRE, "agent");
;             asm volatile("s_waitcnt vmcnt(0)" ::: "memory");
;         }
;     }
;     __syncthreads();
; }
; __device__ __forceinline__ void phase1(const Params& p, LAS unsigned char* lds, const int wave) {
;     ...
;     if (tid < 192) { const int idx = bid * 192 + tid, b = idx / NMOD, j = idx % NMOD; float s = p.b_ada[j];
;         for (int ks = 0; ks < KS_MOD; ++ks) s += p.modp[(size_t)(ks * 4 + b) * NMOD + j];
;         p.mod[idx] = s; }
.LBB0_29:
	s_or_b64 exec, exec, s[0:1]
	s_waitcnt vmcnt(0)
	s_sub_i32 s0, 0, s91
	s_barrier
	v_mbcnt_lo_u32_b32 v0, -1, 0
	v_mbcnt_hi_u32_b32 v0, -1, v0
	v_writelane_b32 v255, s0, 25
	v_cmp_eq_u32_e32 vcc, s0, v0
	s_and_saveexec_b64 s[0:1], vcc
	v_writelane_b32 v255, s46, 26
	s_nop 1
	v_writelane_b32 v255, s47, 27
	v_writelane_b32 v255, s90, 28
	v_writelane_b32 v255, s91, 29
	s_cbranch_execz .LBB0_81
	v_readlane_b32 s30, v254, 36
	v_readlane_b32 s31, v254, 37
	v_readlane_b32 s2, v254, 21
	s_add_u32 s10, s30, 0x1400
	s_addc_u32 s11, s31, 0
	s_and_b32 s2, s2, 7
	s_lshl_b32 s16, s2, 8
	s_lshl_b32 s17, s2, 2
	v_mov_b32_e32 v0, s16
	v_mov_b32_e32 v1, 1
	s_waitcnt vmcnt(0) lgkmcnt(0)
	global_atomic_add v1, v0, v1, s[10:11] sc0
	s_waitcnt vmcnt(0)
	v_readfirstlane_b32 s2, v1
	s_add_u32 s2, s2, 1
	s_cmp_lg_u32 s2, 0x20
	s_cbranch_scc1 .Lmy_gb1_wait
	buffer_wbl2 sc1
	v_mov_b32_e32 v0, s17
	v_mov_b32_e32 v1, 1
	s_waitcnt vmcnt(0)
	global_store_dword v0, v1, s[30:31] sc1
.Lmy_gb1_wait:
	v_mov_b32_e32 v0, 0
	s_mov_b32 s2, 0
.Lmy_gb1_poll:
	global_load_dwordx4 v[2:5], v0, s[30:31] sc1
	global_load_dwordx4 v[6:9], v0, s[30:31] offset:16 sc1
	s_waitcnt vmcnt(0)
	v_min_u32_e32 v2, v2, v3
	v_min_u32_e32 v4, v4, v5
	v_min_u32_e32 v6, v6, v7
	v_min_u32_e32 v8, v8, v9
	v_min_u32_e32 v2, v2, v4
	v_min_u32_e32 v6, v6, v8
	v_min_u32_e32 v1, v2, v6
	v_cmp_gt_u32_e32 vcc, 1, v1
	s_cbranch_vccz .Lmy_gb1_done
	s_sleep 1
	s_add_u32 s2, s2, 1
	s_cmp_lt_u32 s2, 0x40000
	s_cbranch_scc1 .Lmy_gb1_poll
.Lmy_gb1_done:
	buffer_inv sc1
	s_waitcnt vmcnt(0)
.Lmy_gb1_out:
.LBB0_81:
	s_or_b64 exec, exec, s[0:1]
	v_readlane_b32 s0, v254, 2
	s_lshr_b32 s0, s0, 6
	s_waitcnt lgkmcnt(0)
	v_writelane_b32 v255, s0, 30
	s_barrier
	v_mbcnt_lo_u32_b32 v0, -1, 0
	v_mbcnt_hi_u32_b32 v0, -1, v0
	s_movk_i32 s0, 0xc0
	v_add_u32_e32 v22, s91, v0
	v_cmp_gt_i32_e32 vcc, s0, v22
	s_and_saveexec_b64 s[4:5], vcc
	s_cbranch_execz .LBB0_85
	v_readlane_b32 s0, v254, 3
	s_mulk_i32 s0, 0xc0
	v_readlane_b32 s12, v254, 40
	v_add_u32_e32 v0, s0, v22
	s_mov_b32 s0, 0x2aaaaaab
	v_mul_hi_i32 v1, v0, s0
	v_lshrrev_b32_e32 v2, 31, v1
	v_ashrrev_i32_e32 v1, 11, v1
	v_add_u32_e32 v1, v1, v2
	v_mul_i32_i24_e32 v2, 0x3000, v1
	v_sub_u32_e32 v2, v0, v2
	v_ashrrev_i32_e32 v3, 31, v2
	v_lshlrev_b64 v[2:3], 2, v[2:3]
	v_readlane_b32 s18, v254, 46
	v_readlane_b32 s19, v254, 47
	v_readlane_b32 s13, v254, 41
	v_readlane_b32 s14, v254, 42
	v_lshl_add_u64 v[4:5], s[18:19], 0, v[2:3]
	global_load_dword v4, v[4:5], off
	v_readlane_b32 s15, v254, 43
	v_readlane_b32 s16, v254, 44
	v_readlane_b32 s17, v254, 45
	v_readlane_b32 s20, v254, 48
	v_readlane_b32 s21, v254, 49
	v_readlane_b32 s22, v254, 50
	v_readlane_b32 s23, v254, 51
	v_readlane_b32 s24, v254, 52
	v_readlane_b32 s25, v254, 53
	v_readlane_b32 s26, v254, 54
	v_readlane_b32 s27, v254, 55
	v_readlane_b32 s1, v254, 4
	s_mov_b32 s0, 0xc000
	v_readlane_b32 s12, v254, 5
	v_mad_i64_i32 v[2:3], s[0:1], v1, s0, v[2:3]
	v_readlane_b32 s14, v254, 7
	v_readlane_b32 s15, v254, 8
	s_mov_b64 s[6:7], 0
	v_readlane_b32 s13, v254, 6
	v_lshl_add_u64 v[2:3], s[14:15], 0, v[2:3]
	v_readlane_b32 s16, v254, 9
	v_readlane_b32 s17, v254, 10
	v_readlane_b32 s18, v254, 11
	v_readlane_b32 s19, v254, 12
	v_readlane_b32 s20, v254, 13
	v_readlane_b32 s21, v254, 14
	v_readlane_b32 s22, v254, 15
	v_readlane_b32 s23, v254, 16
	v_readlane_b32 s24, v254, 17
	v_readlane_b32 s25, v254, 18
	v_readlane_b32 s26, v254, 19
	v_readlane_b32 s27, v254, 20
	global_load_dword v32, v[2:3], off
	s_mov_b32 s0, 0x30000
	s_mov_b32 s1, 0
	v_lshl_add_u64 v[24:25], v[2:3], 0, s[0:1]
	global_load_dword v33, v[24:25], off
	s_mov_b32 s0, 0x60000
	s_mov_b32 s1, 0
	v_lshl_add_u64 v[24:25], v[2:3], 0, s[0:1]
	global_load_dword v34, v[24:25], off
	s_mov_b32 s0, 0x90000
	s_mov_b32 s1, 0
	v_lshl_add_u64 v[24:25], v[2:3], 0, s[0:1]
	global_load_dword v35, v[24:25], off
	s_mov_b32 s0, 0xc0000
	s_mov_b32 s1, 0
	v_lshl_add_u64 v[24:25], v[2:3], 0, s[0:1]
	global_load_dword v36, v[24:25], off
	s_mov_b32 s0, 0xf0000
	s_mov_b32 s1, 0
	v_lshl_add_u64 v[24:25], v[2:3], 0, s[0:1]
	global_load_dword v37, v[24:25], off
	s_mov_b32 s0, 0x120000
	s_mov_b32 s1, 0
	v_lshl_add_u64 v[24:25], v[2:3], 0, s[0:1]
	global_load_dword v38, v[24:25], off
	s_mov_b32 s0, 0x150000
	s_mov_b32 s1, 0
	v_lshl_add_u64 v[24:25], v[2:3], 0, s[0:1]
	global_load_dword v39, v[24:25], off
	s_mov_b32 s0, 0x180000
	s_mov_b32 s1, 0
	v_lshl_add_u64 v[24:25], v[2:3], 0, s[0:1]
	global_load_dword v40, v[24:25], off
	s_mov_b32 s0, 0x1b0000
	s_mov_b32 s1, 0
	v_lshl_add_u64 v[24:25], v[2:3], 0, s[0:1]
	global_load_dword v41, v[24:25], off
	s_mov_b32 s0, 0x1e0000
	s_mov_b32 s1, 0
	v_lshl_add_u64 v[24:25], v[2:3], 0, s[0:1]
	global_load_dword v42, v[24:25], off
; __device__ __forceinline__ void phase1(const Params& p, LAS unsigned char* lds, const int wave) {
;     ...
;     if (tid < 192) { const int idx = bid * 192 + tid, b = idx / NMOD, j = idx % NMOD; float s = p.b_ada[j];
;         for (int ks = 0; ks < KS_MOD; ++ks) s += p.modp[(size_t)(ks * 4 + b) * NMOD + j];
;         p.mod[idx] = s; }
	s_mov_b32 s0, 0x210000
	s_mov_b32 s1, 0
	v_lshl_add_u64 v[24:25], v[2:3], 0, s[0:1]
	global_load_dword v43, v[24:25], off
	s_mov_b32 s0, 0x240000
	s_mov_b32 s1, 0
	v_lshl_add_u64 v[24:25], v[2:3], 0, s[0:1]
	global_load_dword v44, v[24:25], off
	s_mov_b32 s0, 0x270000
	s_mov_b32 s1, 0
	v_lshl_add_u64 v[24:25], v[2:3], 0, s[0:1]
	global_load_dword v45, v[24:25], off
	s_mov_b32 s0, 0x2a0000
	s_mov_b32 s1, 0
	v_lshl_add_u64 v[24:25], v[2:3], 0, s[0:1]
	global_load_dword v46, v[24:25], off
	s_mov_b32 s0, 0x2d0000
	s_mov_b32 s1, 0
	v_lshl_add_u64 v[24:25], v[2:3], 0, s[0:1]
	global_load_dword v47, v[24:25], off
	s_mov_b32 s0, 0x300000
	s_mov_b32 s1, 0
	v_lshl_add_u64 v[24:25], v[2:3], 0, s[0:1]
	global_load_dword v48, v[24:25], off
	s_mov_b32 s0, 0x330000
	s_mov_b32 s1, 0
	v_lshl_add_u64 v[24:25], v[2:3], 0, s[0:1]
	global_load_dword v49, v[24:25], off
	s_mov_b32 s0, 0x360000
	s_mov_b32 s1, 0
	v_lshl_add_u64 v[24:25], v[2:3], 0, s[0:1]
	global_load_dword v50, v[24:25], off
	s_mov_b32 s0, 0x390000
	s_mov_b32 s1, 0
	v_lshl_add_u64 v[24:25], v[2:3], 0, s[0:1]
	global_load_dword v51, v[24:25], off
	s_mov_b32 s0, 0x3c0000
	s_mov_b32 s1, 0
	v_lshl_add_u64 v[24:25], v[2:3], 0, s[0:1]
	global_load_dword v52, v[24:25], off
	s_mov_b32 s0, 0x3f0000
	s_mov_b32 s1, 0
	v_lshl_add_u64 v[24:25], v[2:3], 0, s[0:1]
	global_load_dword v53, v[24:25], off
	s_mov_b32 s0, 0x420000
	s_mov_b32 s1, 0
	v_lshl_add_u64 v[24:25], v[2:3], 0, s[0:1]
	global_load_dword v54, v[24:25], off
	s_mov_b32 s0, 0x450000
	s_mov_b32 s1, 0
	v_lshl_add_u64 v[24:25], v[2:3], 0, s[0:1]
	global_load_dword v55, v[24:25], off
	s_mov_b32 s0, 0x480000
	s_mov_b32 s1, 0
	v_lshl_add_u64 v[24:25], v[2:3], 0, s[0:1]
	global_load_dword v56, v[24:25], off
	s_mov_b32 s0, 0x4b0000
	s_mov_b32 s1, 0
	v_lshl_add_u64 v[24:25], v[2:3], 0, s[0:1]
	global_load_dword v57, v[24:25], off
	s_mov_b32 s0, 0x4e0000
	s_mov_b32 s1, 0
	v_lshl_add_u64 v[24:25], v[2:3], 0, s[0:1]
	global_load_dword v58, v[24:25], off
	s_mov_b32 s0, 0x510000
	s_mov_b32 s1, 0
	v_lshl_add_u64 v[24:25], v[2:3], 0, s[0:1]
	global_load_dword v59, v[24:25], off
	s_mov_b32 s0, 0x540000
	s_mov_b32 s1, 0
	v_lshl_add_u64 v[24:25], v[2:3], 0, s[0:1]
	global_load_dword v60, v[24:25], off
	s_mov_b32 s0, 0x570000
	s_mov_b32 s1, 0
	v_lshl_add_u64 v[24:25], v[2:3], 0, s[0:1]
	global_load_dword v61, v[24:25], off
	s_mov_b32 s0, 0x5a0000
	s_mov_b32 s1, 0
	v_lshl_add_u64 v[24:25], v[2:3], 0, s[0:1]
	global_load_dword v62, v[24:25], off
	s_mov_b32 s0, 0x5d0000
	s_mov_b32 s1, 0
	v_lshl_add_u64 v[24:25], v[2:3], 0, s[0:1]
	global_load_dword v63, v[24:25], off
	s_waitcnt vmcnt(31)
	v_add_f32_e32 v4, v4, v32
	s_waitcnt vmcnt(30)
	v_add_f32_e32 v4, v4, v33
	s_waitcnt vmcnt(29)
	v_add_f32_e32 v4, v4, v34
	s_waitcnt vmcnt(28)
	v_add_f32_e32 v4, v4, v35
	s_waitcnt vmcnt(27)
	v_add_f32_e32 v4, v4, v36
	s_waitcnt vmcnt(26)
	v_add_f32_e32 v4, v4, v37
	s_waitcnt vmcnt(25)
	v_add_f32_e32 v4, v4, v38
	s_waitcnt vmcnt(24)
	v_add_f32_e32 v4, v4, v39
	s_waitcnt vmcnt(23)
	v_add_f32_e32 v4, v4, v40
	s_waitcnt vmcnt(22)
	v_add_f32_e32 v4, v4, v41
	s_waitcnt vmcnt(21)
	v_add_f32_e32 v4, v4, v42
	s_waitcnt vmcnt(20)
	v_add_f32_e32 v4, v4, v43
	s_waitcnt vmcnt(19)
	v_add_f32_e32 v4, v4, v44
	s_waitcnt vmcnt(18)
	v_add_f32_e32 v4, v4, v45
	s_waitcnt vmcnt(17)
	v_add_f32_e32 v4, v4, v46
	s_waitcnt vmcnt(16)
	v_add_f32_e32 v4, v4, v47
	s_waitcnt vmcnt(15)
	v_add_f32_e32 v4, v4, v48
	s_waitcnt vmcnt(14)
	v_add_f32_e32 v4, v4, v49
	s_waitcnt vmcnt(13)
	v_add_f32_e32 v4, v4, v50
	s_waitcnt vmcnt(12)
	v_add_f32_e32 v4, v4, v51
	s_waitcnt vmcnt(11)
	v_add_f32_e32 v4, v4, v52
	s_waitcnt vmcnt(10)
	v_add_f32_e32 v4, v4, v53
	s_waitcnt vmcnt(9)
	v_add_f32_e32 v4, v4, v54
	s_waitcnt vmcnt(8)
	v_add_f32_e32 v4, v4, v55
	s_waitcnt vmcnt(7)
	v_add_f32_e32 v4, v4, v56
	s_waitcnt vmcnt(6)
	v_add_f32_e32 v4, v4, v57
	s_waitcnt vmcnt(5)
	v_add_f32_e32 v4, v4, v58
	s_waitcnt vmcnt(4)
	v_add_f32_e32 v4, v4, v59
	s_waitcnt vmcnt(3)
	v_add_f32_e32 v4, v4, v60
	s_waitcnt vmcnt(2)
	v_add_f32_e32 v4, v4, v61
	s_waitcnt vmcnt(1)
	v_add_f32_e32 v4, v4, v62
	s_waitcnt vmcnt(0)
	v_add_f32_e32 v4, v4, v63
	v_readlane_b32 s36, v254, 5
	v_ashrrev_i32_e32 v1, 31, v0
	v_readlane_b32 s40, v254, 9
	v_readlane_b32 s41, v254, 10
	v_readlane_b32 s37, v254, 6
	v_readlane_b32 s38, v254, 7
	v_lshl_add_u64 v[0:1], v[0:1], 2, s[40:41]
	v_readlane_b32 s39, v254, 8
	v_readlane_b32 s42, v254, 11
	v_readlane_b32 s43, v254, 12
	v_readlane_b32 s44, v254, 13
	v_readlane_b32 s45, v254, 14
	v_readlane_b32 s46, v254, 15
	v_readlane_b32 s47, v254, 16
	v_readlane_b32 s48, v254, 17
	v_readlane_b32 s49, v254, 18
	v_readlane_b32 s50, v254, 19
	v_readlane_b32 s51, v254, 20
	global_store_dword v[0:1], v4, off

; __device__ __forceinline__ unsigned pack4_fp8(float a, float b, float c, float d) { int r = 0; r = __builtin_amdgcn_cvt_pk_fp8_f32(a, b, r, false); r = __builtin_amdgcn_cvt_pk_fp8_f32(c, d, r, true); return (unsigned)r; }
; __device__ __forceinline__ f32x4 ld4nt(const float* p) { return __builtin_nontemporal_load((const f32x4*)p); }
; __device__ __forceinline__ void phase1(const Params& p, LAS unsigned char* lds, const int wave) {
;     ...
;     for (int i0 = 0; i0 < 16; i0 += 8) {
;         f32x4 xa[8], xc[8];
; #pragma unroll
;         for (int u = 0; u < 8; ++u) { const size_t m = (size_t)(m0 + 2 * (i0 + u) + rh); xa[u] = ld4nt(p.x + m * ND + k); xc[u] = ld4nt(p.x + m * ND + k + 4); }
; #pragma unroll
;         for (int u = 0; u < 8; ++u) { const size_t m = (size_t)(m0 + 2 * (i0 + u) + rh); const f32x4 h0 = xa[u] * sc0 + sh0, h1 = xc[u] * sc1v + sh1v;
;             u32x2 w; w.x = pack4_fp8(h0[0], h0[1], h0[2], h0[3]); w.y = pack4_fp8(h1[0], h1[1], h1[2], h1[3]); *(u32x2*)(p.hb + m * ND + k) = w; } }
.LBB0_88:
	v_add_u32_e32 v22, s2, v24
	v_ashrrev_i32_e32 v23, 31, v22
	v_lshlrev_b64 v[26:27], 13, v[22:23]
	v_lshl_add_u64 v[30:31], v[16:17], 0, v[26:27]
	v_add_u32_e32 v104, 2, v22
	v_add_u32_e32 v106, 4, v22
	v_add_u32_e32 v108, 6, v22
	v_add_u32_e32 v110, 8, v22
	v_add_u32_e32 v112, 10, v22
	v_add_u32_e32 v114, 12, v22
	v_add_u32_e32 v116, 14, v22
	global_load_dwordx4 v[26:29], v[30:31], off nt
	s_nop 0
	global_load_dwordx4 v[30:33], v[30:31], off offset:16 nt
	v_ashrrev_i32_e32 v105, 31, v104
	v_ashrrev_i32_e32 v107, 31, v106
	v_ashrrev_i32_e32 v109, 31, v108
	v_ashrrev_i32_e32 v111, 31, v110
	v_ashrrev_i32_e32 v113, 31, v112
	v_ashrrev_i32_e32 v115, 31, v114
	v_ashrrev_i32_e32 v117, 31, v116
	v_lshlrev_b64 v[34:35], 13, v[104:105]
	v_lshlrev_b64 v[36:37], 13, v[106:107]
	v_lshlrev_b64 v[38:39], 13, v[108:109]
	v_lshlrev_b64 v[40:41], 13, v[110:111]
	v_lshlrev_b64 v[42:43], 13, v[112:113]
	v_lshlrev_b64 v[44:45], 13, v[114:115]
	v_lshlrev_b64 v[46:47], 13, v[116:117]
	v_lshl_add_u64 v[48:49], v[16:17], 0, v[34:35]
	v_lshl_add_u64 v[50:51], v[16:17], 0, v[36:37]
	v_lshl_add_u64 v[54:55], v[16:17], 0, v[38:39]
	v_lshl_add_u64 v[62:63], v[16:17], 0, v[40:41]
	v_lshl_add_u64 v[70:71], v[16:17], 0, v[42:43]
	v_lshl_add_u64 v[78:79], v[16:17], 0, v[44:45]
	v_lshl_add_u64 v[86:87], v[16:17], 0, v[46:47]
	global_load_dwordx4 v[34:37], v[48:49], off nt
	global_load_dwordx4 v[38:41], v[48:49], off offset:16 nt
	global_load_dwordx4 v[42:45], v[50:51], off nt
	s_nop 0
	global_load_dwordx4 v[46:49], v[50:51], off offset:16 nt
	s_nop 0
	global_load_dwordx4 v[50:53], v[54:55], off nt
	s_nop 0
	global_load_dwordx4 v[54:57], v[54:55], off offset:16 nt
	s_nop 0
	global_load_dwordx4 v[58:61], v[62:63], off nt
	s_nop 0
	global_load_dwordx4 v[62:65], v[62:63], off offset:16 nt
	s_nop 0
	global_load_dwordx4 v[66:69], v[70:71], off nt
	s_nop 0
	global_load_dwordx4 v[70:73], v[70:71], off offset:16 nt
	s_nop 0
	global_load_dwordx4 v[74:77], v[78:79], off nt
	s_nop 0
	global_load_dwordx4 v[78:81], v[78:79], off offset:16 nt
	s_nop 0
	global_load_dwordx4 v[82:85], v[86:87], off nt
	s_nop 0
	global_load_dwordx4 v[86:89], v[86:87], off offset:16 nt
	v_mov_b32_e32 v20, 0
	v_mov_b32_e32 v21, 0
	v_mov_b32_e32 v90, 0
	v_mov_b32_e32 v91, 0
	v_mov_b32_e32 v92, 0
	v_mov_b32_e32 v93, 0
	v_mov_b32_e32 v94, 0
	v_mov_b32_e32 v95, 0
	v_mov_b32_e32 v96, 0
	v_mov_b32_e32 v97, 0
	v_mov_b32_e32 v98, 0
	v_mov_b32_e32 v99, 0
	v_mov_b32_e32 v100, 0
	v_mov_b32_e32 v101, 0
	v_mov_b32_e32 v102, 0
	v_mov_b32_e32 v103, 0
	v_lshlrev_b64 v[22:23], 11, v[22:23]
	s_mov_b32 s2, 16
	s_and_b64 vcc, exec, s[0:1]
	s_mov_b64 s[0:1], 0
	v_lshl_add_u64 v[22:23], v[18:19], 0, v[22:23]
	v_lshlrev_b64 v[104:105], 11, v[104:105]
	v_lshlrev_b64 v[106:107], 11, v[106:107]
	v_lshlrev_b64 v[108:109], 11, v[108:109]
	v_lshlrev_b64 v[110:111], 11, v[110:111]
	v_lshlrev_b64 v[112:113], 11, v[112:113]
	v_lshlrev_b64 v[114:115], 11, v[114:115]
	v_lshlrev_b64 v[116:117], 11, v[116:117]
	v_lshl_add_u64 v[104:105], v[18:19], 0, v[104:105]
	v_lshl_add_u64 v[106:107], v[18:19], 0, v[106:107]
	v_lshl_add_u64 v[108:109], v[18:19], 0, v[108:109]
	v_lshl_add_u64 v[110:111], v[18:19], 0, v[110:111]
	v_lshl_add_u64 v[112:113], v[18:19], 0, v[112:113]
	v_lshl_add_u64 v[114:115], v[18:19], 0, v[114:115]
	v_lshl_add_u64 v[116:117], v[18:19], 0, v[116:117]
	s_waitcnt vmcnt(15) lgkmcnt(1)
	v_pk_fma_f32 v[26:27], v[10:11], v[26:27], v[0:1]
	s_waitcnt vmcnt(14) lgkmcnt(0)
	v_pk_fma_f32 v[30:31], v[14:15], v[30:31], v[4:5]
	v_cvt_pk_fp8_f32 v20, v26, v27
	v_cvt_pk_fp8_f32 v21, v30, v31
	v_pk_fma_f32 v[28:29], v[8:9], v[28:29], v[2:3]
	v_pk_fma_f32 v[32:33], v[12:13], v[32:33], v[6:7]
	v_cvt_pk_fp8_f32 v20, v28, v29 op_sel:[0,0,1]
	v_cvt_pk_fp8_f32 v21, v32, v33 op_sel:[0,0,1]
	s_waitcnt vmcnt(13)
	v_pk_fma_f32 v[26:27], v[8:9], v[36:37], v[2:3]
	v_pk_fma_f32 v[30:31], v[10:11], v[34:35], v[0:1]
	s_waitcnt vmcnt(12)
	v_pk_fma_f32 v[36:37], v[14:15], v[38:39], v[4:5]
	v_pk_fma_f32 v[34:35], v[12:13], v[40:41], v[6:7]
	s_waitcnt vmcnt(11)
	v_pk_fma_f32 v[38:39], v[8:9], v[44:45], v[2:3]
	v_pk_fma_f32 v[40:41], v[10:11], v[42:43], v[0:1]
	s_waitcnt vmcnt(10)
	v_pk_fma_f32 v[44:45], v[14:15], v[46:47], v[4:5]
	v_cvt_pk_fp8_f32 v90, v30, v31
	v_cvt_pk_fp8_f32 v91, v36, v37
	v_pk_fma_f32 v[42:43], v[12:13], v[48:49], v[6:7]
	s_waitcnt vmcnt(9)
	v_pk_fma_f32 v[46:47], v[8:9], v[52:53], v[2:3]
	v_pk_fma_f32 v[48:49], v[10:11], v[50:51], v[0:1]
	s_waitcnt vmcnt(8)
	v_pk_fma_f32 v[52:53], v[14:15], v[54:55], v[4:5]
	v_cvt_pk_fp8_f32 v92, v40, v41
	v_cvt_pk_fp8_f32 v93, v44, v45
	v_pk_fma_f32 v[50:51], v[12:13], v[56:57], v[6:7]
	s_waitcnt vmcnt(7)
	v_pk_fma_f32 v[54:55], v[8:9], v[60:61], v[2:3]
	v_pk_fma_f32 v[56:57], v[10:11], v[58:59], v[0:1]
	s_waitcnt vmcnt(6)
	v_pk_fma_f32 v[58:59], v[12:13], v[64:65], v[6:7]
	v_pk_fma_f32 v[60:61], v[14:15], v[62:63], v[4:5]
	s_waitcnt vmcnt(5)
	v_pk_fma_f32 v[62:63], v[8:9], v[68:69], v[2:3]
	v_pk_fma_f32 v[64:65], v[10:11], v[66:67], v[0:1]
	s_waitcnt vmcnt(4)
	v_pk_fma_f32 v[66:67], v[12:13], v[72:73], v[6:7]
	v_pk_fma_f32 v[68:69], v[14:15], v[70:71], v[4:5]
	s_waitcnt vmcnt(3)
	v_pk_fma_f32 v[70:71], v[8:9], v[76:77], v[2:3]
	v_pk_fma_f32 v[72:73], v[10:11], v[74:75], v[0:1]
	s_waitcnt vmcnt(2)
	v_pk_fma_f32 v[74:75], v[12:13], v[80:81], v[6:7]
	v_pk_fma_f32 v[76:77], v[14:15], v[78:79], v[4:5]
	s_waitcnt vmcnt(1)
	v_pk_fma_f32 v[78:79], v[8:9], v[84:85], v[2:3]
	v_pk_fma_f32 v[80:81], v[10:11], v[82:83], v[0:1]
	s_waitcnt vmcnt(0)
	v_pk_fma_f32 v[84:85], v[14:15], v[86:87], v[4:5]
	v_cvt_pk_fp8_f32 v94, v48, v49
	v_cvt_pk_fp8_f32 v95, v52, v53
	v_cvt_pk_fp8_f32 v96, v56, v57
	v_cvt_pk_fp8_f32 v97, v60, v61
	v_cvt_pk_fp8_f32 v98, v64, v65
	v_cvt_pk_fp8_f32 v99, v68, v69
	v_cvt_pk_fp8_f32 v100, v72, v73
	v_cvt_pk_fp8_f32 v101, v76, v77
	v_cvt_pk_fp8_f32 v102, v80, v81
	v_cvt_pk_fp8_f32 v103, v84, v85
	v_cvt_pk_fp8_f32 v90, v26, v27 op_sel:[0,0,1]
	v_cvt_pk_fp8_f32 v91, v34, v35 op_sel:[0,0,1]
	v_cvt_pk_fp8_f32 v92, v38, v39 op_sel:[0,0,1]
	v_cvt_pk_fp8_f32 v93, v42, v43 op_sel:[0,0,1]
	v_pk_fma_f32 v[82:83], v[12:13], v[88:89], v[6:7]
	v_cvt_pk_fp8_f32 v94, v46, v47 op_sel:[0,0,1]
	v_cvt_pk_fp8_f32 v95, v50, v51 op_sel:[0,0,1]
	v_cvt_pk_fp8_f32 v96, v54, v55 op_sel:[0,0,1]
	v_cvt_pk_fp8_f32 v97, v58, v59 op_sel:[0,0,1]
	v_cvt_pk_fp8_f32 v98, v62, v63 op_sel:[0,0,1]
	v_cvt_pk_fp8_f32 v99, v66, v67 op_sel:[0,0,1]
	v_cvt_pk_fp8_f32 v100, v70, v71 op_sel:[0,0,1]
	v_cvt_pk_fp8_f32 v101, v74, v75 op_sel:[0,0,1]
	v_cvt_pk_fp8_f32 v102, v78, v79 op_sel:[0,0,1]
	v_cvt_pk_fp8_f32 v103, v82, v83 op_sel:[0,0,1]
	global_store_dwordx2 v[22:23], v[20:21], off
	global_store_dwordx2 v[104:105], v[90:91], off
	global_store_dwordx2 v[106:107], v[92:93], off
	global_store_dwordx2 v[108:109], v[94:95], off
	global_store_dwordx2 v[110:111], v[96:97], off
	global_store_dwordx2 v[112:113], v[98:99], off
	global_store_dwordx2 v[114:115], v[100:101], off
	global_store_dwordx2 v[116:117], v[102:103], off
	s_cbranch_vccnz .LBB0_88
; __device__ __forceinline__ unsigned xb_ld(unsigned* p)              { return __hip_atomic_load(p, __ATOMIC_RELAXED, __HIP_MEMORY_SCOPE_AGENT); }
; __device__ __forceinline__ unsigned xb_add(unsigned* p, unsigned v) { return __hip_atomic_fetch_add(p, v, __ATOMIC_RELAXED, __HIP_MEMORY_SCOPE_AGENT); }
; #define XB_SPIN(cond, bar) do { unsigned _sp = 0; while (cond) { __builtin_amdgcn_s_sleep(1); \
;     if ((++_sp & 255u) == 0u) { if (xb_ld(&(bar)[XB_TMO])) break; if (_sp > XB_SPIN_CAP) { atomicAdd(&(bar)[XB_TMO], 1u); break; } } } } while (0)
; __device__ __forceinline__ void xcd_barrier(const XcdBarrier& b, const int wave) {
;     asm volatile("s_waitcnt vmcnt(0)" ::: "memory");
;     __syncthreads();
;     if (phase_tid(wave) == 0) {
;         unsigned* bar = b.bar;
;         __builtin_amdgcn_s_waitcnt(0);
;         unsigned nloc = b.st[0], nx = b.st[1];
;         if (nloc == 0u) { xcd_barrier_complete(bar, b.x, nloc, nx); b.st[0] = nloc; b.st[1] = nx; }
;         const unsigned old = xb_add(&bar[XB_XSUB(b.x)], 1u);
;         const unsigned gen = old / nloc;
;         if (old + 1u == (gen + 1u) * nloc) {
;             __builtin_amdgcn_fence(__ATOMIC_RELEASE, "agent");
;             asm volatile("s_waitcnt vmcnt(0)" ::: "memory");
;             const unsigned og = xb_add(&bar[XB_TOP], 1u);
;             const unsigned tg = og / nx;
;             if (og + 1u == (tg + 1u) * nx) xb_add(&bar[XB_TOPGEN], 1u);
;             else XB_SPIN(xb_ld(&bar[XB_TOPGEN]) == tg, bar);
;             __builtin_amdgcn_fence(__ATOMIC_ACQUIRE, "agent");
;             xb_add(&bar[XB_XGEN(b.x)], 1u);
;             asm volatile("s_waitcnt vmcnt(0)" ::: "memory");
;         } else {
;             XB_SPIN(xb_ld(&bar[XB_XGEN(b.x)]) == gen, bar);
;             __builtin_amdgcn_fence(__ATOMIC_ACQUIRE, "agent");
;             asm volatile("s_waitcnt vmcnt(0)" ::: "memory");
;         }
;     }
;     __syncthreads();
; }
	s_barrier
	s_waitcnt vmcnt(0)
	v_readlane_b32 s0, v255, 25
	s_barrier
	v_mbcnt_lo_u32_b32 v0, -1, 0
	v_mbcnt_hi_u32_b32 v0, -1, v0
	s_nop 0
	v_cmp_eq_u32_e32 vcc, s0, v0
	s_and_saveexec_b64 s[0:1], vcc
	s_cbranch_execz .LBB0_141
	v_readlane_b32 s30, v254, 36
	v_readlane_b32 s31, v254, 37
	v_readlane_b32 s2, v254, 21
	s_add_u32 s10, s30, 0x1400
	s_addc_u32 s11, s31, 0
	s_and_b32 s2, s2, 7
	s_lshl_b32 s16, s2, 8
	s_lshl_b32 s17, s2, 2
	v_mov_b32_e32 v0, s16
	v_mov_b32_e32 v1, 1
	s_waitcnt vmcnt(0) lgkmcnt(0)
	global_atomic_add v1, v0, v1, s[10:11] sc0
	s_waitcnt vmcnt(0)
	v_readfirstlane_b32 s2, v1
	s_add_u32 s2, s2, 1
	s_cmp_lg_u32 s2, 0x40
	s_cbranch_scc1 .Lmy_gb2_wait
	buffer_wbl2 sc1
	v_mov_b32_e32 v0, s17
	v_mov_b32_e32 v1, 2
	s_waitcnt vmcnt(0)
	global_store_dword v0, v1, s[30:31] sc1

; __device__ __forceinline__ unsigned xb_ld(unsigned* p)              { return __hip_atomic_load(p, __ATOMIC_RELAXED, __HIP_MEMORY_SCOPE_AGENT); }
; __device__ __forceinline__ unsigned xb_add(unsigned* p, unsigned v) { return __hip_atomic_fetch_add(p, v, __ATOMIC_RELAXED, __HIP_MEMORY_SCOPE_AGENT); }
; #define XB_SPIN(cond, bar) do { unsigned _sp = 0; while (cond) { __builtin_amdgcn_s_sleep(1); \
;     if ((++_sp & 255u) == 0u) { if (xb_ld(&(bar)[XB_TMO])) break; if (_sp > XB_SPIN_CAP) { atomicAdd(&(bar)[XB_TMO], 1u); break; } } } } while (0)
; __device__ __forceinline__ void xcd_barrier(const XcdBarrier& b, const int wave) {
;     asm volatile("s_waitcnt vmcnt(0)" ::: "memory");
;     __syncthreads();
;     if (phase_tid(wave) == 0) {
;         unsigned* bar = b.bar;
;         __builtin_amdgcn_s_waitcnt(0);
;         unsigned nloc = b.st[0], nx = b.st[1];
;         if (nloc == 0u) { xcd_barrier_complete(bar, b.x, nloc, nx); b.st[0] = nloc; b.st[1] = nx; }
;         const unsigned old = xb_add(&bar[XB_XSUB(b.x)], 1u);
;         const unsigned gen = old / nloc;
;         if (old + 1u == (gen + 1u) * nloc) {
;             __builtin_amdgcn_fence(__ATOMIC_RELEASE, "agent");
;             asm volatile("s_waitcnt vmcnt(0)" ::: "memory");
;             const unsigned og = xb_add(&bar[XB_TOP], 1u);
;             const unsigned tg = og / nx;
;             if (og + 1u == (tg + 1u) * nx) xb_add(&bar[XB_TOPGEN], 1u);
;             else XB_SPIN(xb_ld(&bar[XB_TOPGEN]) == tg, bar);
;             __builtin_amdgcn_fence(__ATOMIC_ACQUIRE, "agent");
;             xb_add(&bar[XB_XGEN(b.x)], 1u);
;             asm volatile("s_waitcnt vmcnt(0)" ::: "memory");
;         } else {
;             XB_SPIN(xb_ld(&bar[XB_XGEN(b.x)]) == gen, bar);
;             __builtin_amdgcn_fence(__ATOMIC_ACQUIRE, "agent");
;             asm volatile("s_waitcnt vmcnt(0)" ::: "memory");
;         }
;     }
;     __syncthreads();
; }
.Lmy_gb2_poll:
	global_load_dwordx4 v[2:5], v0, s[30:31] sc1
	global_load_dwordx4 v[6:9], v0, s[30:31] offset:16 sc1
	s_waitcnt vmcnt(0)
	v_min_u32_e32 v2, v2, v3
	v_min_u32_e32 v4, v4, v5
	v_min_u32_e32 v6, v6, v7
	v_min_u32_e32 v8, v8, v9
	v_min_u32_e32 v2, v2, v4
	v_min_u32_e32 v6, v6, v8
	v_min_u32_e32 v1, v2, v6
	v_cmp_gt_u32_e32 vcc, 2, v1
	s_cbranch_vccz .Lmy_gb2_done
	s_sleep 1
	s_add_u32 s2, s2, 1
	s_cmp_lt_u32 s2, 0x40000
	s_cbranch_scc1 .Lmy_gb2_poll

; #define PG8_STAGE(bufoff, rs, soff, voff) do { _Pragma("unroll") for (int _i = 0; _i < 2; ++_i) \
;         __builtin_amdgcn_raw_ptr_buffer_load_lds(rs, (LAS void*)(lds + (bufoff) + ldsw + _i * 8192), 16, (voff), (soff) + _i * ((&(voff) == &voffA) ? pieceA : pieceB), 0, 0); } while (0)
; template <class Epi, class Sched, bool FP8 = false>
; __device__ __forceinline__ void gemm_phase(LAS unsigned char* lds, const Gemm g, const Sched& S, const Epi& E, const int wave) {
;     const int tid = phase_tid(wave);
;     const int wid = __builtin_amdgcn_readfirstlane(tid >> 6), lane = tid & 63, wr = wid >> 2, wc = wid & 3, fr = lane & 15, fq = lane >> 4;
;     const int K = g.K, nt = K / BK;
;     unsigned voffA, voffB;
;     {   int R, C; stage_rc(tid * 16, R, C); const int Rb = Epi::PERM ? ((R & ~31) + perm32(R & 31)) : R;
;         voffA = (unsigned)(R * g.lda + C) * 2u; voffB = (unsigned)(Rb * g.ldb + C) * 2u; }
;     const unsigned pieceA = 64u * (unsigned)g.lda * 2u, pieceB = 64u * (unsigned)g.ldb * 2u;
;     const unsigned kstep = (unsigned)(BK * 2);
;     const unsigned hstepA = (unsigned)HALF * g.lda * 2u, hstepB = (unsigned)HALF * g.ldb * 2u;
;     const __amdgpu_buffer_rsrc_t rsA = __builtin_amdgcn_make_buffer_rsrc((void*)g.A, (short)0, -1, 0x00020000), rsB = __builtin_amdgcn_make_buffer_rsrc((void*)g.Bt, (short)0, -1, 0x00020000);
;     const unsigned ldsw = (unsigned)wid * 1024u;
;     const int aoff = lds_byte(wr * 64 + fr, fq * 8), boff = lds_byte(wc * 32 + fr, fq * 8);
;     ...
;     Unit cur, nxt; int ui = 0;
;     if (!S.next(0, cur)) return;
;     f32x4 acc[2][2][4][2];
; #pragma unroll
;     for (int a = 0; a < 2; ++a)
; #pragma unroll
;         for (int b = 0; b < 2; ++b)
; #pragma unroll
;             for (int m = 0; m < 4; ++m)
; #pragma unroll
;                 for (int n = 0; n < 2; ++n) acc[a][b][m][n] = (f32x4){0.f, 0.f, 0.f, 0.f};
;     bf16x8 At[4][2], B0[2][2], B1[2][2];
;     unsigned cA = cur.aoff, cB = cur.boff;
;     PG8_STAGE(PG8_SB(0, 0), rsB, cB, voffB); PG8_STAGE(PG8_SA(0, 0), rsA, cA, voffA); PG8_STAGE(PG8_SB(0, 1), rsB, cB + hstepB, voffB); PG8_STAGE(PG8_SA(0, 1), rsA, cA + hstepA, voffA);
;     if (wr == 1) PG8_BAR;
;     PG8_WAIT_V(4); PG8_BAR;
;     PG8_STAGE(PG8_SB(1, 0), rsB, cB + kstep, voffB); PG8_STAGE(PG8_SA(1, 0), rsA, cA + kstep, voffA); PG8_STAGE(PG8_SB(1, 1), rsB, cB + hstepB + kstep, voffB);
;     PG8_WAIT_V(6); PG8_BAR;
.Lmy_gb2_out:
.LBB0_141:
	s_or_b64 exec, exec, s[0:1]
	s_waitcnt lgkmcnt(0)
	s_barrier
	v_mbcnt_lo_u32_b32 v0, -1, 0
	v_mbcnt_hi_u32_b32 v0, -1, v0
	s_and_b32 s89, s89, 0xffff
	v_add_u32_e32 v1, s91, v0
	s_and_b32 s9, s9, 0xffff
	v_readlane_b32 s0, v254, 3
	v_readfirstlane_b32 s16, v1
	s_mov_b32 s91, 0x20000
	s_cmpk_gt_u32 s0, 0x3ff
	s_mov_b32 s90, -1
	v_readlane_b32 s1, v254, 4
	s_cbranch_scc1 .LBB0_157
	v_ashrrev_i32_e32 v3, 31, v1
	v_lshrrev_b32_e32 v3, 26, v3
	v_lshlrev_b32_e32 v2, 4, v1
	v_add_u32_e32 v3, v1, v3
	v_bfe_i32 v1, v1, 27, 1
	v_lshrrev_b32_e32 v1, 22, v1
	v_add_u32_e32 v1, v2, v1
	v_and_b32_e32 v1, 0xfffffc00, v1
	v_sub_u32_e32 v1, v2, v1
	v_lshrrev_b32_e32 v2, 4, v1
	v_bitop3_b32 v1, v2, v1, 32 bitop3:0x6c
	v_ashrrev_i32_e32 v4, 31, v1
	v_ashrrev_i32_e32 v3, 6, v3
	v_lshrrev_b32_e32 v4, 26, v4
	v_lshlrev_b32_e32 v2, 3, v3
	v_add_u32_e32 v4, v1, v4
	v_and_b32_e32 v2, -16, v2
	v_ashrrev_i32_e32 v5, 6, v4
	v_add_u32_e32 v2, v5, v2
	v_and_b32_e32 v5, 3, v5
	s_mov_b32 s3, 0x1fffe0
	v_and_or_b32 v5, v2, s3, v5
	v_readlane_b32 s2, v254, 3
	v_readlane_b32 s3, v254, 4
	s_lshr_b32 s3, s2, 3
	s_lshl_b32 s5, s2, 7
	s_lshl_b32 s6, s2, 2
	s_ashr_i32 s0, s16, 6
	s_and_b32 s6, s6, 24
	s_or_b32 s3, s5, s3
	s_bfe_u32 s5, s2, 0x30003
	s_ashr_i32 s1, s16, 8
	v_and_b32_e32 v4, 0xc0, v4
	s_lshl_b32 s4, s0, 10
	s_or_b32 s93, s6, s5
	s_bfe_u32 s5, s3, 0x50003
	s_and_b32 s3, s3, 0xff
	v_sub_u32_e32 v1, v1, v4
	v_mov_b32_e32 v4, 1
	s_cmpk_lt_u32 s3, 0xb8
	v_lshlrev_b32_e32 v3, 5, v3
	v_ashrrev_i16_sdwa v1, v4, sext(v1) dst_sel:DWORD dst_unused:UNUSED_PAD src0_sel:DWORD src1_sel:BYTE_0
	v_lshlrev_b32_e32 v4, 1, v2
	v_lshrrev_b32_e32 v6, 2, v2
	s_cselect_b32 s3, 0, 2
	v_and_b32_e32 v3, 32, v3
	v_bfe_i32 v1, v1, 0, 16
	v_and_b32_e32 v4, 24, v4
	v_and_b32_e32 v6, 4, v6
	s_add_i32 s94, s3, s5
	s_add_i32 s5, s4, 0
	v_or3_b32 v4, v5, v6, v4
	v_add_lshl_u32 v1, v3, v1, 1
	s_add_i32 s12, s5, 0x10000
	v_lshl_add_u32 v131, v4, 11, v1
	s_lshl_b32 s3, s94, 19
	s_mov_b32 s10, s90
	s_mov_b32 s11, s91
	s_mov_b32 m0, s12
	s_add_i32 s13, s5, 0x12000
	buffer_load_dwordx4 v131, s[8:11], s3 offen lds
	s_or_b32 s4, s3, 0x20000
	s_mov_b32 m0, s13
	v_lshl_add_u32 v130, v2, 11, v1
	s_lshl_b32 s96, s93, 19
	buffer_load_dwordx4 v131, s[8:11], s4 offen lds
	s_mov_b32 m0, s5
	s_add_i32 s14, s5, 0x2000
	buffer_load_dwordx4 v130, s[88:91], s96 offen lds
	s_or_b32 s4, s96, 0x20000
	s_mov_b32 m0, s14
	s_add_i32 s15, s5, 0x14000
	buffer_load_dwordx4 v130, s[88:91], s4 offen lds
	s_or_b32 s4, s3, 0x40000
	s_mov_b32 m0, s15
	s_add_i32 s33, s5, 0x16000
	buffer_load_dwordx4 v131, s[8:11], s4 offen lds
	s_or_b32 s4, s3, 0x60000
	s_mov_b32 m0, s33
	s_add_i32 s34, s5, 0x4000
	buffer_load_dwordx4 v131, s[8:11], s4 offen lds
	s_or_b32 s4, s96, 0x40000
	s_mov_b32 m0, s34
	s_add_i32 s35, s5, 0x6000
	buffer_load_dwordx4 v130, s[88:91], s4 offen lds
	s_or_b32 s4, s96, 0x60000
	s_mov_b32 m0, s35
	s_cmp_lg_u32 s1, 1
	buffer_load_dwordx4 v130, s[88:91], s4 offen lds
	s_mov_b32 s36, 0
	s_cbranch_scc1 .LBB0_144
	s_barrier

; __device__ __forceinline__ unsigned xb_ld(unsigned* p)              { return __hip_atomic_load(p, __ATOMIC_RELAXED, __HIP_MEMORY_SCOPE_AGENT); }
; __device__ __forceinline__ unsigned xb_add(unsigned* p, unsigned v) { return __hip_atomic_fetch_add(p, v, __ATOMIC_RELAXED, __HIP_MEMORY_SCOPE_AGENT); }
; #define XB_SPIN(cond, bar) do { unsigned _sp = 0; while (cond) { __builtin_amdgcn_s_sleep(1); \
;     if ((++_sp & 255u) == 0u) { if (xb_ld(&(bar)[XB_TMO])) break; if (_sp > XB_SPIN_CAP) { atomicAdd(&(bar)[XB_TMO], 1u); break; } } } } while (0)
; __device__ __forceinline__ void xcd_barrier(const XcdBarrier& b, const int wave) {
;     asm volatile("s_waitcnt vmcnt(0)" ::: "memory");
;     __syncthreads();
;     if (phase_tid(wave) == 0) {
;         unsigned* bar = b.bar;
;         __builtin_amdgcn_s_waitcnt(0);
;         unsigned nloc = b.st[0], nx = b.st[1];
;         if (nloc == 0u) { xcd_barrier_complete(bar, b.x, nloc, nx); b.st[0] = nloc; b.st[1] = nx; }
;         const unsigned old = xb_add(&bar[XB_XSUB(b.x)], 1u);
;         const unsigned gen = old / nloc;
;         if (old + 1u == (gen + 1u) * nloc) {
;             __builtin_amdgcn_fence(__ATOMIC_RELEASE, "agent");
;             asm volatile("s_waitcnt vmcnt(0)" ::: "memory");
;             const unsigned og = xb_add(&bar[XB_TOP], 1u);
;             const unsigned tg = og / nx;
;             if (og + 1u == (tg + 1u) * nx) xb_add(&bar[XB_TOPGEN], 1u);
;             else XB_SPIN(xb_ld(&bar[XB_TOPGEN]) == tg, bar);
;             __builtin_amdgcn_fence(__ATOMIC_ACQUIRE, "agent");
;             xb_add(&bar[XB_XGEN(b.x)], 1u);
;             asm volatile("s_waitcnt vmcnt(0)" ::: "memory");
;         } else {
;             XB_SPIN(xb_ld(&bar[XB_XGEN(b.x)]) == gen, bar);
;             __builtin_amdgcn_fence(__ATOMIC_ACQUIRE, "agent");
;             asm volatile("s_waitcnt vmcnt(0)" ::: "memory");
;         }
;     }
;     __syncthreads();
; }
.LBB0_157:
	s_waitcnt vmcnt(0)
	v_readlane_b32 s0, v255, 25
	s_waitcnt vmcnt(16)
	s_barrier
	v_mbcnt_lo_u32_b32 v0, -1, 0
	v_mbcnt_hi_u32_b32 v0, -1, v0
	s_nop 0
	v_cmp_eq_u32_e32 vcc, s0, v0
	s_and_saveexec_b64 s[0:1], vcc
	s_cbranch_execz .LBB0_209
	v_readlane_b32 s30, v254, 36
	v_readlane_b32 s31, v254, 37
	v_readlane_b32 s2, v254, 21
	s_add_u32 s10, s30, 0x1400
	s_addc_u32 s11, s31, 0
	s_and_b32 s2, s2, 7
	s_lshl_b32 s16, s2, 8
	s_lshl_b32 s17, s2, 2
	v_mov_b32_e32 v0, s16
	v_mov_b32_e32 v1, 1
	s_waitcnt vmcnt(0) lgkmcnt(0)
	global_atomic_add v1, v0, v1, s[10:11] sc0
	s_waitcnt vmcnt(0)
	v_readfirstlane_b32 s2, v1
	s_add_u32 s2, s2, 1
	s_cmp_lg_u32 s2, 0x60
	s_cbranch_scc1 .Lmy_gb3_wait
	buffer_wbl2 sc1
	v_mov_b32_e32 v0, s17
	v_mov_b32_e32 v1, 3
	s_waitcnt vmcnt(0)
	global_store_dword v0, v1, s[30:31] sc1

; __device__ __forceinline__ unsigned xb_ld(unsigned* p)              { return __hip_atomic_load(p, __ATOMIC_RELAXED, __HIP_MEMORY_SCOPE_AGENT); }
; __device__ __forceinline__ unsigned xb_add(unsigned* p, unsigned v) { return __hip_atomic_fetch_add(p, v, __ATOMIC_RELAXED, __HIP_MEMORY_SCOPE_AGENT); }
; #define XB_SPIN(cond, bar) do { unsigned _sp = 0; while (cond) { __builtin_amdgcn_s_sleep(1); \
;     if ((++_sp & 255u) == 0u) { if (xb_ld(&(bar)[XB_TMO])) break; if (_sp > XB_SPIN_CAP) { atomicAdd(&(bar)[XB_TMO], 1u); break; } } } } while (0)
; __device__ __forceinline__ void xcd_barrier(const XcdBarrier& b, const int wave) {
;     asm volatile("s_waitcnt vmcnt(0)" ::: "memory");
;     __syncthreads();
;     if (phase_tid(wave) == 0) {
;         unsigned* bar = b.bar;
;         __builtin_amdgcn_s_waitcnt(0);
;         unsigned nloc = b.st[0], nx = b.st[1];
;         if (nloc == 0u) { xcd_barrier_complete(bar, b.x, nloc, nx); b.st[0] = nloc; b.st[1] = nx; }
;         const unsigned old = xb_add(&bar[XB_XSUB(b.x)], 1u);
;         const unsigned gen = old / nloc;
;         if (old + 1u == (gen + 1u) * nloc) {
;             __builtin_amdgcn_fence(__ATOMIC_RELEASE, "agent");
;             asm volatile("s_waitcnt vmcnt(0)" ::: "memory");
;             const unsigned og = xb_add(&bar[XB_TOP], 1u);
;             const unsigned tg = og / nx;
;             if (og + 1u == (tg + 1u) * nx) xb_add(&bar[XB_TOPGEN], 1u);
;             else XB_SPIN(xb_ld(&bar[XB_TOPGEN]) == tg, bar);
;             __builtin_amdgcn_fence(__ATOMIC_ACQUIRE, "agent");
;             xb_add(&bar[XB_XGEN(b.x)], 1u);
;             asm volatile("s_waitcnt vmcnt(0)" ::: "memory");
;         } else {
;             XB_SPIN(xb_ld(&bar[XB_XGEN(b.x)]) == gen, bar);
;             __builtin_amdgcn_fence(__ATOMIC_ACQUIRE, "agent");
;             asm volatile("s_waitcnt vmcnt(0)" ::: "memory");
;         }
;     }
;     __syncthreads();
; }
.Lmy_gb3_poll:
	global_load_dwordx4 v[2:5], v0, s[30:31] sc1
	global_load_dwordx4 v[6:9], v0, s[30:31] offset:16 sc1
	s_waitcnt vmcnt(0)
	v_min_u32_e32 v2, v2, v3
	v_min_u32_e32 v4, v4, v5
	v_min_u32_e32 v6, v6, v7
	v_min_u32_e32 v8, v8, v9
	v_min_u32_e32 v2, v2, v4
	v_min_u32_e32 v6, v6, v8
	v_min_u32_e32 v1, v2, v6
	v_cmp_gt_u32_e32 vcc, 3, v1
	s_cbranch_vccz .Lmy_gb3_done
	s_sleep 1
	s_add_u32 s2, s2, 1
	s_cmp_lt_u32 s2, 0x40000
	s_cbranch_scc1 .Lmy_gb3_poll

; #define LAS __attribute__((address_space(3)))
; __device__ __forceinline__ unsigned xb_ld(unsigned* p)              { return __hip_atomic_load(p, __ATOMIC_RELAXED, __HIP_MEMORY_SCOPE_AGENT); }
; __device__ __forceinline__ unsigned xb_add(unsigned* p, unsigned v) { return __hip_atomic_fetch_add(p, v, __ATOMIC_RELAXED, __HIP_MEMORY_SCOPE_AGENT); }
; __device__ __forceinline__ void xcd_barrier(const XcdBarrier& b, const int wave) {
;     asm volatile("s_waitcnt vmcnt(0)" ::: "memory");
;     __syncthreads();
;     if (phase_tid(wave) == 0) {
;         unsigned* bar = b.bar;
;         __builtin_amdgcn_s_waitcnt(0);
;         unsigned nloc = b.st[0], nx = b.st[1];
;         if (nloc == 0u) { xcd_barrier_complete(bar, b.x, nloc, nx); b.st[0] = nloc; b.st[1] = nx; }
;         const unsigned old = xb_add(&bar[XB_XSUB(b.x)], 1u);
;         const unsigned gen = old / nloc;
;         if (old + 1u == (gen + 1u) * nloc) {
;             __builtin_amdgcn_fence(__ATOMIC_RELEASE, "agent");
;             asm volatile("s_waitcnt vmcnt(0)" ::: "memory");
;             const unsigned og = xb_add(&bar[XB_TOP], 1u);
;             const unsigned tg = og / nx;
;             if (og + 1u == (tg + 1u) * nx) xb_add(&bar[XB_TOPGEN], 1u);
;             else XB_SPIN(xb_ld(&bar[XB_TOPGEN]) == tg, bar);
;             __builtin_amdgcn_fence(__ATOMIC_ACQUIRE, "agent");
;             xb_add(&bar[XB_XGEN(b.x)], 1u);
;             asm volatile("s_waitcnt vmcnt(0)" ::: "memory");
;         } else {
;             XB_SPIN(xb_ld(&bar[XB_XGEN(b.x)]) == gen, bar);
;             __builtin_amdgcn_fence(__ATOMIC_ACQUIRE, "agent");
;             asm volatile("s_waitcnt vmcnt(0)" ::: "memory");
;         }
;     }
;     __syncthreads();
; }
; __device__ __forceinline__ void phase3(const Params& p, LAS unsigned char* lds, const int wave) {
;     ...
;     const int bid = blockIdx.x, m0 = bid * 32, t0 = m0 & (NT - 1), hist = t0 > 0 ? 15 : 0;
;     constexpr int TC = OFF_GA - OFF_WD, TCH = TC / 8;
;     LAS bf16_t* T = (LAS bf16_t*)lds;
; #pragma unroll 1
;     for (int i0 = 0; i0 < 16; i0 += 8) {
;         u32x4 tv[8];
; #pragma unroll
;         for (int u = 0; u < 8; ++u) { const int idx = tid + (i0 + u) * NTHREADS, r = idx / TCH, ck = idx % TCH; tv[u] = (u32x4){0u, 0u, 0u, 0u};
;             if (idx < 47 * TCH && r >= 15 - hist) tv[u] = ldu4nt(p.P + (size_t)(m0 - 15 + r) * NINP + OFF_WD + ck * 8); }
.Lmy_gb3_out:
.LBB0_209:
	s_or_b64 exec, exec, s[0:1]
	v_readlane_b32 s1, v255, 33
	s_and_b32 s3, s1, 0x7e0
	v_readlane_b32 s0, v255, 29
	s_cmp_eq_u32 s3, 0
	s_waitcnt lgkmcnt(0)
	s_barrier
	v_mbcnt_lo_u32_b32 v39, -1, 0
	v_mbcnt_hi_u32_b32 v39, -1, v39
	s_cselect_b32 s33, 15, 0
	v_add_u32_e32 v38, s0, v39
	s_mov_b32 s0, 0
	s_add_i32 s34, s1, -15
	s_mov_b64 s[4:5], -1
	s_mov_b32 s35, 0x63e7063f
	s_movk_i32 s36, 0x1e1c
	s_movk_i32 s37, 0xa4
	s_movk_i32 s42, 0x4400
	s_movk_i32 s43, 0xa40
	s_branch .LBB0_211

; __device__ __forceinline__ unsigned xb_ld(unsigned* p)              { return __hip_atomic_load(p, __ATOMIC_RELAXED, __HIP_MEMORY_SCOPE_AGENT); }
; __device__ __forceinline__ unsigned xb_add(unsigned* p, unsigned v) { return __hip_atomic_fetch_add(p, v, __ATOMIC_RELAXED, __HIP_MEMORY_SCOPE_AGENT); }
; #define XB_SPIN(cond, bar) do { unsigned _sp = 0; while (cond) { __builtin_amdgcn_s_sleep(1); \
;     if ((++_sp & 255u) == 0u) { if (xb_ld(&(bar)[XB_TMO])) break; if (_sp > XB_SPIN_CAP) { atomicAdd(&(bar)[XB_TMO], 1u); break; } } } } while (0)
; __device__ __forceinline__ void xcd_barrier(const XcdBarrier& b, const int wave) {
;     asm volatile("s_waitcnt vmcnt(0)" ::: "memory");
;     __syncthreads();
;     if (phase_tid(wave) == 0) {
;         unsigned* bar = b.bar;
;         __builtin_amdgcn_s_waitcnt(0);
;         unsigned nloc = b.st[0], nx = b.st[1];
;         if (nloc == 0u) { xcd_barrier_complete(bar, b.x, nloc, nx); b.st[0] = nloc; b.st[1] = nx; }
;         const unsigned old = xb_add(&bar[XB_XSUB(b.x)], 1u);
;         const unsigned gen = old / nloc;
;         if (old + 1u == (gen + 1u) * nloc) {
;             __builtin_amdgcn_fence(__ATOMIC_RELEASE, "agent");
;             asm volatile("s_waitcnt vmcnt(0)" ::: "memory");
;             const unsigned og = xb_add(&bar[XB_TOP], 1u);
;             const unsigned tg = og / nx;
;             if (og + 1u == (tg + 1u) * nx) xb_add(&bar[XB_TOPGEN], 1u);
;             else XB_SPIN(xb_ld(&bar[XB_TOPGEN]) == tg, bar);
;             __builtin_amdgcn_fence(__ATOMIC_ACQUIRE, "agent");
;             xb_add(&bar[XB_XGEN(b.x)], 1u);
;             asm volatile("s_waitcnt vmcnt(0)" ::: "memory");
;         } else {
;             XB_SPIN(xb_ld(&bar[XB_XGEN(b.x)]) == gen, bar);
;             __builtin_amdgcn_fence(__ATOMIC_ACQUIRE, "agent");
;             asm volatile("s_waitcnt vmcnt(0)" ::: "memory");
;         }
;     }
;     __syncthreads();
; }
.LBB0_370:
	s_or_b64 exec, exec, s[0:1]
	s_barrier
	s_waitcnt vmcnt(0)
	v_readlane_b32 s0, v255, 25
	s_barrier
	v_mbcnt_lo_u32_b32 v0, -1, 0
	v_mbcnt_hi_u32_b32 v0, -1, v0
	s_nop 0
	v_cmp_eq_u32_e32 vcc, s0, v0
	s_and_saveexec_b64 s[0:1], vcc
	s_cbranch_execz .LBB0_422
	v_readlane_b32 s30, v254, 36
	v_readlane_b32 s31, v254, 37
	v_readlane_b32 s2, v254, 21
	s_add_u32 s10, s30, 0x1400
	s_addc_u32 s11, s31, 0
	s_and_b32 s2, s2, 7
	s_lshl_b32 s16, s2, 8
	s_lshl_b32 s17, s2, 2
	v_mov_b32_e32 v0, s16
	v_mov_b32_e32 v1, 1
	s_waitcnt vmcnt(0) lgkmcnt(0)
	global_atomic_add v1, v0, v1, s[10:11] sc0
	s_waitcnt vmcnt(0)
	v_readfirstlane_b32 s2, v1
	s_add_u32 s2, s2, 1
	s_cmp_lg_u32 s2, 0x80
	s_cbranch_scc1 .Lmy_gb4_wait
	buffer_wbl2 sc1
	v_mov_b32_e32 v0, s17
	v_mov_b32_e32 v1, 4
	s_waitcnt vmcnt(0)
	global_store_dword v0, v1, s[30:31] sc1

; __device__ __forceinline__ unsigned xb_ld(unsigned* p)              { return __hip_atomic_load(p, __ATOMIC_RELAXED, __HIP_MEMORY_SCOPE_AGENT); }
; __device__ __forceinline__ unsigned xb_add(unsigned* p, unsigned v) { return __hip_atomic_fetch_add(p, v, __ATOMIC_RELAXED, __HIP_MEMORY_SCOPE_AGENT); }
; #define XB_SPIN(cond, bar) do { unsigned _sp = 0; while (cond) { __builtin_amdgcn_s_sleep(1); \
;     if ((++_sp & 255u) == 0u) { if (xb_ld(&(bar)[XB_TMO])) break; if (_sp > XB_SPIN_CAP) { atomicAdd(&(bar)[XB_TMO], 1u); break; } } } } while (0)
; __device__ __forceinline__ void xcd_barrier(const XcdBarrier& b, const int wave) {
;     asm volatile("s_waitcnt vmcnt(0)" ::: "memory");
;     __syncthreads();
;     if (phase_tid(wave) == 0) {
;         unsigned* bar = b.bar;
;         __builtin_amdgcn_s_waitcnt(0);
;         unsigned nloc = b.st[0], nx = b.st[1];
;         if (nloc == 0u) { xcd_barrier_complete(bar, b.x, nloc, nx); b.st[0] = nloc; b.st[1] = nx; }
;         const unsigned old = xb_add(&bar[XB_XSUB(b.x)], 1u);
;         const unsigned gen = old / nloc;
;         if (old + 1u == (gen + 1u) * nloc) {
;             __builtin_amdgcn_fence(__ATOMIC_RELEASE, "agent");
;             asm volatile("s_waitcnt vmcnt(0)" ::: "memory");
;             const unsigned og = xb_add(&bar[XB_TOP], 1u);
;             const unsigned tg = og / nx;
;             if (og + 1u == (tg + 1u) * nx) xb_add(&bar[XB_TOPGEN], 1u);
;             else XB_SPIN(xb_ld(&bar[XB_TOPGEN]) == tg, bar);
;             __builtin_amdgcn_fence(__ATOMIC_ACQUIRE, "agent");
;             xb_add(&bar[XB_XGEN(b.x)], 1u);
;             asm volatile("s_waitcnt vmcnt(0)" ::: "memory");
;         } else {
;             XB_SPIN(xb_ld(&bar[XB_XGEN(b.x)]) == gen, bar);
;             __builtin_amdgcn_fence(__ATOMIC_ACQUIRE, "agent");
;             asm volatile("s_waitcnt vmcnt(0)" ::: "memory");
;         }
;     }
;     __syncthreads();
; }
.Lmy_gb4_poll:
	global_load_dwordx4 v[2:5], v0, s[30:31] sc1
	global_load_dwordx4 v[6:9], v0, s[30:31] offset:16 sc1
	s_waitcnt vmcnt(0)
	v_min_u32_e32 v2, v2, v3
	v_min_u32_e32 v4, v4, v5
	v_min_u32_e32 v6, v6, v7
	v_min_u32_e32 v8, v8, v9
	v_min_u32_e32 v2, v2, v4
	v_min_u32_e32 v6, v6, v8
	v_min_u32_e32 v1, v2, v6
	v_cmp_gt_u32_e32 vcc, 4, v1
	s_cbranch_vccz .Lmy_gb4_done
	s_sleep 1
	s_add_u32 s2, s2, 1
	s_cmp_lt_u32 s2, 0x40000
	s_cbranch_scc1 .Lmy_gb4_poll

; template <class Epi, class Sched, bool FP8 = false>
; __device__ __forceinline__ void gemm_phase(LAS unsigned char* lds, const Gemm g, const Sched& S, const Epi& E, const int wave) {
;     const int tid = phase_tid(wave);
;     const int wid = __builtin_amdgcn_readfirstlane(tid >> 6), lane = tid & 63, wr = wid >> 2, wc = wid & 3, fr = lane & 15, fq = lane >> 4;
;     const int K = g.K, nt = K / BK;
;     unsigned voffA, voffB;
;     {   int R, C; stage_rc(tid * 16, R, C); const int Rb = Epi::PERM ? ((R & ~31) + perm32(R & 31)) : R;
;         voffA = (unsigned)(R * g.lda + C) * 2u; voffB = (unsigned)(Rb * g.ldb + C) * 2u; }
;     const unsigned pieceA = 64u * (unsigned)g.lda * 2u, pieceB = 64u * (unsigned)g.ldb * 2u;
;     const unsigned kstep = (unsigned)(BK * 2);
;     const unsigned hstepA = (unsigned)HALF * g.lda * 2u, hstepB = (unsigned)HALF * g.ldb * 2u;
;     const __amdgpu_buffer_rsrc_t rsA = __builtin_amdgcn_make_buffer_rsrc((void*)g.A, (short)0, -1, 0x00020000), rsB = __builtin_amdgcn_make_buffer_rsrc((void*)g.Bt, (short)0, -1, 0x00020000);
;     const unsigned ldsw = (unsigned)wid * 1024u;
;     const int aoff = lds_byte(wr * 64 + fr, fq * 8), boff = lds_byte(wc * 32 + fr, fq * 8);
;     ...
;     Unit cur, nxt; int ui = 0;
;     if (!S.next(0, cur)) return;
;     f32x4 acc[2][2][4][2];
; #pragma unroll
;     for (int a = 0; a < 2; ++a)
; #pragma unroll
;         for (int b = 0; b < 2; ++b)
; #pragma unroll
;             for (int m = 0; m < 4; ++m)
; #pragma unroll
;                 for (int n = 0; n < 2; ++n) acc[a][b][m][n] = (f32x4){0.f, 0.f, 0.f, 0.f};
;     bf16x8 At[4][2], B0[2][2], B1[2][2];
;     unsigned cA = cur.aoff, cB = cur.boff;
;     PG8_STAGE(PG8_SB(0, 0), rsB, cB, voffB); PG8_STAGE(PG8_SA(0, 0), rsA, cA, voffA); PG8_STAGE(PG8_SB(0, 1), rsB, cB + hstepB, voffB); PG8_STAGE(PG8_SA(0, 1), rsA, cA + hstepA, voffA);
;     if (wr == 1) PG8_BAR;
;     PG8_WAIT_V(4); PG8_BAR;
;     PG8_STAGE(PG8_SB(1, 0), rsB, cB + kstep, voffB); PG8_STAGE(PG8_SA(1, 0), rsA, cA + kstep, voffA); PG8_STAGE(PG8_SB(1, 1), rsB, cB + hstepB + kstep, voffB);
;     PG8_WAIT_V(6); PG8_BAR;
;     __device__ bool next(int i, Unit& u) const {
;         if (i > 0 || c < 0 || c >= 64) return false;
;         u.pm = c >> 1; u.pn = 23 + (c & 1); u.e = 0; u.aoff = (unsigned)((size_t)u.pm * a_tile); u.boff = (unsigned)((size_t)u.pn * b_tile); return true;
.Lmy_gb4_out:
.LBB0_422:
	s_or_b64 exec, exec, s[0:1]
	v_readlane_b32 s0, v255, 29
	s_waitcnt lgkmcnt(0)
	s_barrier
	v_mbcnt_lo_u32_b32 v0, -1, 0
	v_mbcnt_hi_u32_b32 v0, -1, v0
	v_readlane_b32 s10, v254, 3
	v_add_u32_e32 v1, s0, v0
	s_cmp_gt_u32 s10, 63
	v_readfirstlane_b32 s1, v1
	v_readlane_b32 s11, v254, 4
	s_cbranch_scc1 .LBB0_430
	v_ashrrev_i32_e32 v3, 31, v1
	v_lshrrev_b32_e32 v3, 26, v3
	v_lshlrev_b32_e32 v2, 4, v1
	v_add_u32_e32 v3, v1, v3
	v_bfe_i32 v1, v1, 27, 1
	v_lshrrev_b32_e32 v1, 22, v1
	v_add_u32_e32 v1, v2, v1
	v_and_b32_e32 v1, 0xfffffc00, v1
	v_sub_u32_e32 v1, v2, v1
	v_lshrrev_b32_e32 v2, 4, v1
	v_bitop3_b32 v1, v2, v1, 32 bitop3:0x6c
	v_ashrrev_i32_e32 v4, 31, v1
	v_ashrrev_i32_e32 v3, 6, v3
	v_lshrrev_b32_e32 v4, 26, v4
	v_lshlrev_b32_e32 v2, 3, v3
	v_add_u32_e32 v4, v1, v4
	v_and_b32_e32 v2, -16, v2
	v_ashrrev_i32_e32 v5, 6, v4
	v_and_b32_e32 v4, 0xc0, v4
	s_ashr_i32 s2, s1, 6
	v_add_u32_e32 v2, v5, v2
	v_sub_u32_e32 v1, v1, v4
	v_mov_b32_e32 v4, 1
	v_lshlrev_b32_e32 v3, 5, v3
	v_ashrrev_i16_sdwa v1, v4, sext(v1) dst_sel:DWORD dst_unused:UNUSED_PAD src0_sel:DWORD src1_sel:BYTE_0
	v_lshlrev_b32_e32 v4, 1, v2
	v_lshrrev_b32_e32 v6, 2, v2
	v_and_b32_e32 v5, 3, v5
	s_mov_b32 s0, 0x1fffe0
	s_lshl_b32 s6, s2, 10
	v_and_b32_e32 v3, 32, v3
	v_bfe_i32 v1, v1, 0, 16
	v_and_b32_e32 v4, 24, v4
	v_and_b32_e32 v6, 4, v6
	v_and_or_b32 v5, v2, s0, v5
	s_and_b32 s3, s10, 1
	s_add_i32 s6, s6, 0
	v_or3_b32 v4, v5, v6, v4
	v_add_lshl_u32 v1, v3, v1, 1
	s_add_i32 s3, s3, 23
	s_add_i32 s7, s6, 0x10000
	v_lshl_add_u32 v129, v4, 11, v1
	s_lshr_b32 s0, s10, 1
	s_lshl_b32 s5, s3, 19
	s_mov_b32 s10, s90
	s_mov_b32 s11, s91
	s_mov_b32 m0, s7
	s_add_i32 s14, s6, 0x12000
	buffer_load_dwordx4 v129, s[8:11], s5 offen lds
	s_or_b32 s15, s5, 0x20000
	s_mov_b32 m0, s14
	v_lshl_add_u32 v128, v2, 11, v1
	s_lshl_b32 s4, s0, 19
	buffer_load_dwordx4 v129, s[8:11], s15 offen lds
	s_mov_b32 m0, s6
	s_add_i32 s15, s6, 0x2000
	buffer_load_dwordx4 v128, s[88:91], s4 offen lds
	s_or_b32 s33, s4, 0x20000
	s_mov_b32 m0, s15
	s_or_b32 s34, s5, 0x40000
	buffer_load_dwordx4 v128, s[88:91], s33 offen lds
	s_add_i32 s33, s6, 0x14000
	s_mov_b32 m0, s33
	s_or_b32 s35, s5, 0x60000
	buffer_load_dwordx4 v129, s[8:11], s34 offen lds
	s_add_i32 s34, s6, 0x16000
	s_mov_b32 m0, s34
	s_or_b32 s36, s4, 0x40000
	buffer_load_dwordx4 v129, s[8:11], s35 offen lds
	s_add_i32 s35, s6, 0x4000
	s_mov_b32 m0, s35
	s_or_b32 s37, s4, 0x60000
	buffer_load_dwordx4 v128, s[88:91], s36 offen lds
	s_add_i32 s36, s6, 0x6000
	s_mov_b32 m0, s36
	s_ashr_i32 s38, s1, 8
	buffer_load_dwordx4 v128, s[88:91], s37 offen lds
	s_cmp_lg_u32 s38, 1
	s_cbranch_scc1 .LBB0_425
	s_barrier

; __device__ __forceinline__ unsigned xb_ld(unsigned* p)              { return __hip_atomic_load(p, __ATOMIC_RELAXED, __HIP_MEMORY_SCOPE_AGENT); }
; __device__ __forceinline__ unsigned xb_add(unsigned* p, unsigned v) { return __hip_atomic_fetch_add(p, v, __ATOMIC_RELAXED, __HIP_MEMORY_SCOPE_AGENT); }
; #define XB_SPIN(cond, bar) do { unsigned _sp = 0; while (cond) { __builtin_amdgcn_s_sleep(1); \
;     if ((++_sp & 255u) == 0u) { if (xb_ld(&(bar)[XB_TMO])) break; if (_sp > XB_SPIN_CAP) { atomicAdd(&(bar)[XB_TMO], 1u); break; } } } } while (0)
; __device__ __forceinline__ void xcd_barrier(const XcdBarrier& b, const int wave) {
;     asm volatile("s_waitcnt vmcnt(0)" ::: "memory");
;     __syncthreads();
;     if (phase_tid(wave) == 0) {
;         unsigned* bar = b.bar;
;         __builtin_amdgcn_s_waitcnt(0);
;         unsigned nloc = b.st[0], nx = b.st[1];
;         if (nloc == 0u) { xcd_barrier_complete(bar, b.x, nloc, nx); b.st[0] = nloc; b.st[1] = nx; }
;         const unsigned old = xb_add(&bar[XB_XSUB(b.x)], 1u);
;         const unsigned gen = old / nloc;
;         if (old + 1u == (gen + 1u) * nloc) {
;             __builtin_amdgcn_fence(__ATOMIC_RELEASE, "agent");
;             asm volatile("s_waitcnt vmcnt(0)" ::: "memory");
;             const unsigned og = xb_add(&bar[XB_TOP], 1u);
;             const unsigned tg = og / nx;
;             if (og + 1u == (tg + 1u) * nx) xb_add(&bar[XB_TOPGEN], 1u);
;             else XB_SPIN(xb_ld(&bar[XB_TOPGEN]) == tg, bar);
;             __builtin_amdgcn_fence(__ATOMIC_ACQUIRE, "agent");
;             xb_add(&bar[XB_XGEN(b.x)], 1u);
;             asm volatile("s_waitcnt vmcnt(0)" ::: "memory");
;         } else {
;             XB_SPIN(xb_ld(&bar[XB_XGEN(b.x)]) == gen, bar);
;             __builtin_amdgcn_fence(__ATOMIC_ACQUIRE, "agent");
;             asm volatile("s_waitcnt vmcnt(0)" ::: "memory");
;         }
;     }
;     __syncthreads();
; }
.LBB0_711:
	s_waitcnt vmcnt(0)
	v_readlane_b32 s0, v255, 25
	s_barrier
	v_mbcnt_lo_u32_b32 v0, -1, 0
	v_mbcnt_hi_u32_b32 v0, -1, v0
	s_nop 0
	v_cmp_eq_u32_e32 vcc, s0, v0
	s_and_saveexec_b64 s[0:1], vcc
	s_cbranch_execz .LBB0_763
	v_readlane_b32 s30, v254, 36
	v_readlane_b32 s31, v254, 37
	v_readlane_b32 s2, v254, 21
	s_add_u32 s10, s30, 0x1400
	s_addc_u32 s11, s31, 0
	s_and_b32 s2, s2, 7
	s_lshl_b32 s16, s2, 8
	s_lshl_b32 s17, s2, 2
	v_mov_b32_e32 v0, s16
	v_mov_b32_e32 v1, 1
	s_waitcnt vmcnt(0) lgkmcnt(0)
	global_atomic_add v1, v0, v1, s[10:11] sc0
	s_waitcnt vmcnt(0)
	v_readfirstlane_b32 s2, v1
	s_add_u32 s2, s2, 1
	s_cmp_lg_u32 s2, 0xa0
	s_cbranch_scc1 .Lmy_gb5_wait
	buffer_wbl2 sc1
	v_mov_b32_e32 v0, s17
	v_mov_b32_e32 v1, 5
	s_waitcnt vmcnt(0)
	global_store_dword v0, v1, s[30:31] sc1
.Lmy_gb5_wait:
	v_readlane_b32 s2, v254, 3
	s_cmp_gt_u32 s2, 63
	s_cbranch_scc1 .Lmy_gb5_out
	v_mov_b32_e32 v0, 0
	s_mov_b32 s2, 0
.Lmy_gb5_poll:
	global_load_dwordx4 v[2:5], v0, s[30:31] sc1
	global_load_dwordx4 v[6:9], v0, s[30:31] offset:16 sc1
	s_waitcnt vmcnt(0)
	v_min_u32_e32 v2, v2, v3
	v_min_u32_e32 v4, v4, v5
	v_min_u32_e32 v6, v6, v7
	v_min_u32_e32 v8, v8, v9
	v_min_u32_e32 v2, v2, v4
	v_min_u32_e32 v6, v6, v8
	v_min_u32_e32 v1, v2, v6
	v_cmp_gt_u32_e32 vcc, 5, v1
	s_cbranch_vccz .Lmy_gb5_done
	s_sleep 1
	s_add_u32 s2, s2, 1
	s_cmp_lt_u32 s2, 0x40000
	s_cbranch_scc1 .Lmy_gb5_poll

; #define LAS __attribute__((address_space(3)))
; __device__ __forceinline__ unsigned xb_ld(unsigned* p)              { return __hip_atomic_load(p, __ATOMIC_RELAXED, __HIP_MEMORY_SCOPE_AGENT); }
; __device__ __forceinline__ void xcd_barrier(const XcdBarrier& b, const int wave) {
;     asm volatile("s_waitcnt vmcnt(0)" ::: "memory");
;     __syncthreads();
;     if (phase_tid(wave) == 0) {
;         unsigned* bar = b.bar;
;         __builtin_amdgcn_s_waitcnt(0);
;         unsigned nloc = b.st[0], nx = b.st[1];
;         if (nloc == 0u) { xcd_barrier_complete(bar, b.x, nloc, nx); b.st[0] = nloc; b.st[1] = nx; }
;         const unsigned old = xb_add(&bar[XB_XSUB(b.x)], 1u);
;         const unsigned gen = old / nloc;
;         if (old + 1u == (gen + 1u) * nloc) {
;             __builtin_amdgcn_fence(__ATOMIC_RELEASE, "agent");
;             asm volatile("s_waitcnt vmcnt(0)" ::: "memory");
;             const unsigned og = xb_add(&bar[XB_TOP], 1u);
;             const unsigned tg = og / nx;
;             if (og + 1u == (tg + 1u) * nx) xb_add(&bar[XB_TOPGEN], 1u);
;             else XB_SPIN(xb_ld(&bar[XB_TOPGEN]) == tg, bar);
;             __builtin_amdgcn_fence(__ATOMIC_ACQUIRE, "agent");
;             xb_add(&bar[XB_XGEN(b.x)], 1u);
;             asm volatile("s_waitcnt vmcnt(0)" ::: "memory");
;         } else {
;             XB_SPIN(xb_ld(&bar[XB_XGEN(b.x)]) == gen, bar);
;             __builtin_amdgcn_fence(__ATOMIC_ACQUIRE, "agent");
;             asm volatile("s_waitcnt vmcnt(0)" ::: "memory");
;         }
;     }
;     __syncthreads();
; }
; __device__ __forceinline__ void scan_head(const Params& p, LAS unsigned char* lds, int bh, const int wave) {
;     ...
;     const int b = bh >> 4, h = bh & 15;
;     constexpr int L_AW = 0, L_W = 16384, L_BK = 32768, L_Y = 65536, L_V = 81920, L_G = 106496, L_SC = 131072, L_CS = 131840, L_Z = 132352, L_DUMMY = 132864, L_CST = 133888;
;     constexpr int NCH = NT / 32;
;     if (tid < 128) *(LAS unsigned*)(lds + L_Z + tid * 4) = 0u;
;     {
;         const int a8 = tid >> 6, cc = tid & 63, gch = h * HS + cc;
;         const float* src = a8 == 0 ? p.mu_shift + OFF_R : a8 == 1 ? p.mu_shift + OFF_K : a8 == 2 ? p.mu_shift + OFF_V : a8 == 3 ? p.k_k : a8 == 4 ? p.k_a : a8 == 5 ? p.r_k : a8 == 6 ? p.lnx_g : p.lnx_b;
;         *(LAS float*)(lds + L_CST + a8 * 256 + cc * 4) = src[gch]; }
.Lmy_gb5_out:
.LBB0_763:
	s_or_b64 exec, exec, s[0:1]
	v_readlane_b32 s0, v254, 3
	s_cmp_gt_i32 s0, 63
	s_waitcnt lgkmcnt(0)
	s_barrier
	v_readlane_b32 s1, v254, 4
	s_cbranch_scc1 .LBB0_815
	v_mbcnt_lo_u32_b32 v108, -1, 0
	v_mbcnt_hi_u32_b32 v108, -1, v108
	s_movk_i32 s0, 0x80
	v_add_u32_e32 v109, s62, v108
	v_cmp_gt_i32_e32 vcc, s0, v109
	s_and_saveexec_b64 s[0:1], vcc
	v_lshl_add_u32 v0, v109, 2, 0
	v_add_u32_e32 v0, 0x20500, v0
	v_mov_b32_e32 v1, 0
	ds_write_b32 v0, v1
	s_or_b64 exec, exec, s[0:1]
	v_readlane_b32 s0, v254, 40
	v_readlane_b32 s10, v254, 50
	v_readlane_b32 s11, v254, 51
	v_ashrrev_i32_e32 v2, 6, v109
	v_cmp_lt_u32_e32 vcc, 63, v109
	v_readlane_b32 s1, v254, 41
	v_mov_b64_e32 v[0:1], s[10:11]
	v_readlane_b32 s2, v254, 42
	v_readlane_b32 s3, v254, 43
	v_readlane_b32 s4, v254, 44
	v_readlane_b32 s5, v254, 45
	v_readlane_b32 s6, v254, 46
	v_readlane_b32 s7, v254, 47
	v_readlane_b32 s8, v254, 48
	v_readlane_b32 s9, v254, 49
	v_readlane_b32 s12, v254, 52
	v_readlane_b32 s13, v254, 53
	v_readlane_b32 s14, v254, 54
	v_readlane_b32 s15, v254, 55
	s_and_saveexec_b64 s[0:1], vcc
	s_cbranch_execz .LBB0_773
	v_cmp_lt_i32_e32 vcc, 3, v2
	s_mov_b64 s[4:5], 0
	s_mov_b64 s[8:9], 0
	s_and_saveexec_b64 s[2:3], vcc
	s_xor_b64 s[6:7], exec, s[2:3]
	s_cbranch_execnz .LBB0_855
	s_andn2_saveexec_b64 s[6:7], s[6:7]
	s_cbranch_execnz .LBB0_866

; __device__ __forceinline__ unsigned xb_ld(unsigned* p)              { return __hip_atomic_load(p, __ATOMIC_RELAXED, __HIP_MEMORY_SCOPE_AGENT); }
; __device__ __forceinline__ unsigned xb_add(unsigned* p, unsigned v) { return __hip_atomic_fetch_add(p, v, __ATOMIC_RELAXED, __HIP_MEMORY_SCOPE_AGENT); }
; #define XB_SPIN(cond, bar) do { unsigned _sp = 0; while (cond) { __builtin_amdgcn_s_sleep(1); \
;     if ((++_sp & 255u) == 0u) { if (xb_ld(&(bar)[XB_TMO])) break; if (_sp > XB_SPIN_CAP) { atomicAdd(&(bar)[XB_TMO], 1u); break; } } } } while (0)
; __device__ __forceinline__ void xcd_barrier(const XcdBarrier& b, const int wave) {
;     asm volatile("s_waitcnt vmcnt(0)" ::: "memory");
;     __syncthreads();
;     if (phase_tid(wave) == 0) {
;         unsigned* bar = b.bar;
;         __builtin_amdgcn_s_waitcnt(0);
;         unsigned nloc = b.st[0], nx = b.st[1];
;         if (nloc == 0u) { xcd_barrier_complete(bar, b.x, nloc, nx); b.st[0] = nloc; b.st[1] = nx; }
;         const unsigned old = xb_add(&bar[XB_XSUB(b.x)], 1u);
;         const unsigned gen = old / nloc;
;         if (old + 1u == (gen + 1u) * nloc) {
;             __builtin_amdgcn_fence(__ATOMIC_RELEASE, "agent");
;             asm volatile("s_waitcnt vmcnt(0)" ::: "memory");
;             const unsigned og = xb_add(&bar[XB_TOP], 1u);
;             const unsigned tg = og / nx;
;             if (og + 1u == (tg + 1u) * nx) xb_add(&bar[XB_TOPGEN], 1u);
;             else XB_SPIN(xb_ld(&bar[XB_TOPGEN]) == tg, bar);
;             __builtin_amdgcn_fence(__ATOMIC_ACQUIRE, "agent");
;             xb_add(&bar[XB_XGEN(b.x)], 1u);
;             asm volatile("s_waitcnt vmcnt(0)" ::: "memory");
;         } else {
;             XB_SPIN(xb_ld(&bar[XB_XGEN(b.x)]) == gen, bar);
;             __builtin_amdgcn_fence(__ATOMIC_ACQUIRE, "agent");
;             asm volatile("s_waitcnt vmcnt(0)" ::: "memory");
;         }
;     }
;     __syncthreads();
; }
.LBB0_827:
	s_waitcnt vmcnt(0)
	v_readlane_b32 s0, v255, 25
	s_barrier
	v_mbcnt_lo_u32_b32 v0, -1, 0
	v_mbcnt_hi_u32_b32 v0, -1, v0
	s_nop 0
	v_cmp_eq_u32_e32 vcc, s0, v0
	s_and_saveexec_b64 s[0:1], vcc
	v_readlane_b32 s90, v255, 26
	v_readlane_b32 s91, v255, 27
	v_readlane_b32 s60, v255, 36
	v_readlane_b32 s89, v255, 28
	v_readlane_b32 s91, v255, 29
	v_readlane_b32 s62, v255, 38
	v_readlane_b32 s63, v255, 39
	v_readlane_b32 s64, v255, 40
	v_readlane_b32 s65, v255, 41
	v_readlane_b32 s66, v255, 42
	v_readlane_b32 s67, v255, 43
	v_readlane_b32 s68, v255, 44
	v_readlane_b32 s69, v255, 45
	v_readlane_b32 s70, v255, 46
	v_readlane_b32 s71, v255, 47
	v_readlane_b32 s72, v255, 48
	v_readlane_b32 s73, v255, 49
	v_readlane_b32 s74, v255, 50
	v_readlane_b32 s75, v255, 51
	v_readlane_b32 s61, v255, 37
	s_cbranch_execz .LBB0_898
	v_readlane_b32 s30, v254, 36
	v_readlane_b32 s31, v254, 37
	v_readlane_b32 s2, v254, 21
	s_add_u32 s10, s30, 0x1400
	s_addc_u32 s11, s31, 0
	s_and_b32 s2, s2, 7
	s_lshl_b32 s16, s2, 8
	s_lshl_b32 s17, s2, 2
	v_mov_b32_e32 v0, s16
	v_mov_b32_e32 v1, 1
	s_waitcnt vmcnt(0) lgkmcnt(0)
	global_atomic_add v1, v0, v1, s[10:11] sc0
	s_waitcnt vmcnt(0)
	v_readfirstlane_b32 s2, v1
	s_add_u32 s2, s2, 1
	s_cmp_lg_u32 s2, 0xc0
	s_cbranch_scc1 .Lmy_gb6_wait
	buffer_wbl2 sc1
	v_mov_b32_e32 v0, s17
	v_mov_b32_e32 v1, 6
	s_waitcnt vmcnt(0)
	global_store_dword v0, v1, s[30:31] sc1

; __device__ __forceinline__ unsigned xb_ld(unsigned* p)              { return __hip_atomic_load(p, __ATOMIC_RELAXED, __HIP_MEMORY_SCOPE_AGENT); }
; __device__ __forceinline__ unsigned xb_add(unsigned* p, unsigned v) { return __hip_atomic_fetch_add(p, v, __ATOMIC_RELAXED, __HIP_MEMORY_SCOPE_AGENT); }
; #define XB_SPIN(cond, bar) do { unsigned _sp = 0; while (cond) { __builtin_amdgcn_s_sleep(1); \
;     if ((++_sp & 255u) == 0u) { if (xb_ld(&(bar)[XB_TMO])) break; if (_sp > XB_SPIN_CAP) { atomicAdd(&(bar)[XB_TMO], 1u); break; } } } } while (0)
; __device__ __forceinline__ void xcd_barrier(const XcdBarrier& b, const int wave) {
;     asm volatile("s_waitcnt vmcnt(0)" ::: "memory");
;     __syncthreads();
;     if (phase_tid(wave) == 0) {
;         unsigned* bar = b.bar;
;         __builtin_amdgcn_s_waitcnt(0);
;         unsigned nloc = b.st[0], nx = b.st[1];
;         if (nloc == 0u) { xcd_barrier_complete(bar, b.x, nloc, nx); b.st[0] = nloc; b.st[1] = nx; }
;         const unsigned old = xb_add(&bar[XB_XSUB(b.x)], 1u);
;         const unsigned gen = old / nloc;
;         if (old + 1u == (gen + 1u) * nloc) {
;             __builtin_amdgcn_fence(__ATOMIC_RELEASE, "agent");
;             asm volatile("s_waitcnt vmcnt(0)" ::: "memory");
;             const unsigned og = xb_add(&bar[XB_TOP], 1u);
;             const unsigned tg = og / nx;
;             if (og + 1u == (tg + 1u) * nx) xb_add(&bar[XB_TOPGEN], 1u);
;             else XB_SPIN(xb_ld(&bar[XB_TOPGEN]) == tg, bar);
;             __builtin_amdgcn_fence(__ATOMIC_ACQUIRE, "agent");
;             xb_add(&bar[XB_XGEN(b.x)], 1u);
;             asm volatile("s_waitcnt vmcnt(0)" ::: "memory");
;         } else {
;             XB_SPIN(xb_ld(&bar[XB_XGEN(b.x)]) == gen, bar);
;             __builtin_amdgcn_fence(__ATOMIC_ACQUIRE, "agent");
;             asm volatile("s_waitcnt vmcnt(0)" ::: "memory");
;         }
;     }
;     __syncthreads();
; }
.Lmy_gb6_poll:
	global_load_dwordx4 v[2:5], v0, s[30:31] sc1
	global_load_dwordx4 v[6:9], v0, s[30:31] offset:16 sc1
	s_waitcnt vmcnt(0)
	v_min_u32_e32 v2, v2, v3
	v_min_u32_e32 v4, v4, v5
	v_min_u32_e32 v6, v6, v7
	v_min_u32_e32 v8, v8, v9
	v_min_u32_e32 v2, v2, v4
	v_min_u32_e32 v6, v6, v8
	v_min_u32_e32 v1, v2, v6
	v_cmp_gt_u32_e32 vcc, 6, v1
	s_cbranch_vccz .Lmy_gb6_done
	s_sleep 1
	s_add_u32 s2, s2, 1
	s_cmp_lt_u32 s2, 0x40000
	s_cbranch_scc1 .Lmy_gb6_poll

; __device__ __forceinline__ unsigned xb_ld(unsigned* p)              { return __hip_atomic_load(p, __ATOMIC_RELAXED, __HIP_MEMORY_SCOPE_AGENT); }
; __device__ __forceinline__ unsigned xb_add(unsigned* p, unsigned v) { return __hip_atomic_fetch_add(p, v, __ATOMIC_RELAXED, __HIP_MEMORY_SCOPE_AGENT); }
; #define XB_SPIN(cond, bar) do { unsigned _sp = 0; while (cond) { __builtin_amdgcn_s_sleep(1); \
;     if ((++_sp & 255u) == 0u) { if (xb_ld(&(bar)[XB_TMO])) break; if (_sp > XB_SPIN_CAP) { atomicAdd(&(bar)[XB_TMO], 1u); break; } } } } while (0)
; __device__ __forceinline__ void xcd_barrier(const XcdBarrier& b, const int wave) {
;     asm volatile("s_waitcnt vmcnt(0)" ::: "memory");
;     __syncthreads();
;     if (phase_tid(wave) == 0) {
;         unsigned* bar = b.bar;
;         __builtin_amdgcn_s_waitcnt(0);
;         unsigned nloc = b.st[0], nx = b.st[1];
;         if (nloc == 0u) { xcd_barrier_complete(bar, b.x, nloc, nx); b.st[0] = nloc; b.st[1] = nx; }
;         const unsigned old = xb_add(&bar[XB_XSUB(b.x)], 1u);
;         const unsigned gen = old / nloc;
;         if (old + 1u == (gen + 1u) * nloc) {
;             __builtin_amdgcn_fence(__ATOMIC_RELEASE, "agent");
;             asm volatile("s_waitcnt vmcnt(0)" ::: "memory");
;             const unsigned og = xb_add(&bar[XB_TOP], 1u);
;             const unsigned tg = og / nx;
;             if (og + 1u == (tg + 1u) * nx) xb_add(&bar[XB_TOPGEN], 1u);
;             else XB_SPIN(xb_ld(&bar[XB_TOPGEN]) == tg, bar);
;             __builtin_amdgcn_fence(__ATOMIC_ACQUIRE, "agent");
;             xb_add(&bar[XB_XGEN(b.x)], 1u);
;             asm volatile("s_waitcnt vmcnt(0)" ::: "memory");
;         } else {
;             XB_SPIN(xb_ld(&bar[XB_XGEN(b.x)]) == gen, bar);
;             __builtin_amdgcn_fence(__ATOMIC_ACQUIRE, "agent");
;             asm volatile("s_waitcnt vmcnt(0)" ::: "memory");
;         }
;     }
;     __syncthreads();
; }
.Lmy_gb6_out:
	s_branch .LBB0_898

; #define PG8_STAGE(bufoff, rs, soff, voff) do { _Pragma("unroll") for (int _i = 0; _i < 2; ++_i) \
;         __builtin_amdgcn_raw_ptr_buffer_load_lds(rs, (LAS void*)(lds + (bufoff) + ldsw + _i * 8192), 16, (voff), (soff) + _i * ((&(voff) == &voffA) ? pieceA : pieceB), 0, 0); } while (0)
; template <class Epi, class Sched, bool FP8 = false>
; __device__ __forceinline__ void gemm_phase(LAS unsigned char* lds, const Gemm g, const Sched& S, const Epi& E, const int wave) {
;     const int tid = phase_tid(wave);
;     const int wid = __builtin_amdgcn_readfirstlane(tid >> 6), lane = tid & 63, wr = wid >> 2, wc = wid & 3, fr = lane & 15, fq = lane >> 4;
;     const int K = g.K, nt = K / BK;
;     unsigned voffA, voffB;
;     {   int R, C; stage_rc(tid * 16, R, C); const int Rb = Epi::PERM ? ((R & ~31) + perm32(R & 31)) : R;
;         voffA = (unsigned)(R * g.lda + C) * 2u; voffB = (unsigned)(Rb * g.ldb + C) * 2u; }
;     const unsigned pieceA = 64u * (unsigned)g.lda * 2u, pieceB = 64u * (unsigned)g.ldb * 2u;
;     const unsigned kstep = (unsigned)(BK * 2);
;     const unsigned hstepA = (unsigned)HALF * g.lda * 2u, hstepB = (unsigned)HALF * g.ldb * 2u;
;     const __amdgpu_buffer_rsrc_t rsA = __builtin_amdgcn_make_buffer_rsrc((void*)g.A, (short)0, -1, 0x00020000), rsB = __builtin_amdgcn_make_buffer_rsrc((void*)g.Bt, (short)0, -1, 0x00020000);
;     const unsigned ldsw = (unsigned)wid * 1024u;
;     const int aoff = lds_byte(wr * 64 + fr, fq * 8), boff = lds_byte(wc * 32 + fr, fq * 8);
;     ...
;     Unit cur, nxt; int ui = 0;
;     if (!S.next(0, cur)) return;
;     f32x4 acc[2][2][4][2];
; #pragma unroll
;     for (int a = 0; a < 2; ++a)
; #pragma unroll
;         for (int b = 0; b < 2; ++b)
; #pragma unroll
;             for (int m = 0; m < 4; ++m)
; #pragma unroll
;                 for (int n = 0; n < 2; ++n) acc[a][b][m][n] = (f32x4){0.f, 0.f, 0.f, 0.f};
;     bf16x8 At[4][2], B0[2][2], B1[2][2];
;     unsigned cA = cur.aoff, cB = cur.boff;
;     PG8_STAGE(PG8_SB(0, 0), rsB, cB, voffB); PG8_STAGE(PG8_SA(0, 0), rsA, cA, voffA); PG8_STAGE(PG8_SB(0, 1), rsB, cB + hstepB, voffB); PG8_STAGE(PG8_SA(0, 1), rsA, cA + hstepA, voffA);
;     if (wr == 1) PG8_BAR;
;     PG8_WAIT_V(4); PG8_BAR;
;     PG8_STAGE(PG8_SB(1, 0), rsB, cB + kstep, voffB); PG8_STAGE(PG8_SA(1, 0), rsA, cA + kstep, voffA); PG8_STAGE(PG8_SB(1, 1), rsB, cB + hstepB + kstep, voffB);
;     PG8_WAIT_V(6); PG8_BAR;
.LBB0_873:
	v_readlane_b32 s8, v255, 9
	v_readlane_b32 s22, v255, 23
	v_readlane_b32 s23, v255, 24
	v_readlane_b32 s9, v255, 10
	v_readlane_b32 s10, v255, 11
	v_readlane_b32 s11, v255, 12
	v_readlane_b32 s12, v255, 13
	v_readlane_b32 s13, v255, 14
	v_readlane_b32 s14, v255, 15
	v_readlane_b32 s15, v255, 16
	v_readlane_b32 s16, v255, 17
	v_readlane_b32 s17, v255, 18
	v_readlane_b32 s18, v255, 19
	v_readlane_b32 s19, v255, 20
	v_readlane_b32 s20, v255, 21
	v_readlane_b32 s21, v255, 22
	v_mov_b64_e32 v[0:1], s[22:23]
	s_andn2_b64 s[4:5], s[4:5], exec
	s_or_b64 exec, exec, s[6:7]
	s_and_saveexec_b64 s[6:7], s[4:5]
	s_cbranch_execnz .LBB0_771
	s_branch .LBB0_772
.LBB0_898:
	s_or_b64 exec, exec, s[0:1]
	v_readlane_b32 s0, v254, 3
	s_waitcnt lgkmcnt(0)
	s_barrier
	v_mbcnt_lo_u32_b32 v0, -1, 0
	v_mbcnt_hi_u32_b32 v0, -1, v0
	s_cmpk_lt_u32 s0, 0x100
	v_add_u32_e32 v1, s91, v0
	s_mov_b32 s4, s66
	s_mov_b32 s5, s67
	s_cselect_b64 s[6:7], -1, 0
	s_cmpk_gt_u32 s0, 0xff
	v_readfirstlane_b32 s13, v1
	v_readlane_b32 s1, v254, 4
	s_cbranch_scc1 .LBB0_912
	v_ashrrev_i32_e32 v3, 31, v1
	v_lshrrev_b32_e32 v3, 26, v3
	v_lshlrev_b32_e32 v2, 4, v1
	v_add_u32_e32 v3, v1, v3
	v_bfe_i32 v1, v1, 27, 1
	v_lshrrev_b32_e32 v1, 22, v1
	v_add_u32_e32 v1, v2, v1
	v_and_b32_e32 v1, 0xfffffc00, v1
	v_sub_u32_e32 v1, v2, v1
	v_lshrrev_b32_e32 v2, 4, v1
	v_bitop3_b32 v1, v2, v1, 32 bitop3:0x6c
	v_ashrrev_i32_e32 v4, 31, v1
	v_ashrrev_i32_e32 v3, 6, v3
	v_lshrrev_b32_e32 v4, 26, v4
	v_lshlrev_b32_e32 v2, 3, v3
	v_add_u32_e32 v4, v1, v4
	v_readlane_b32 s2, v254, 3
	v_and_b32_e32 v2, -16, v2
	v_ashrrev_i32_e32 v5, 6, v4
	v_and_b32_e32 v4, 0xc0, v4
	v_readlane_b32 s3, v254, 4
	s_mov_b32 s16, s2
	v_readlane_b32 s17, v255, 33
	s_ashr_i32 s0, s13, 6
	v_add_u32_e32 v2, v5, v2
	v_sub_u32_e32 v1, v1, v4
	v_mov_b32_e32 v4, 1
	v_and_b32_e32 v5, 3, v5
	s_mov_b32 s1, 0x3fffe0
	s_lshr_b32 s2, s2, 3
	s_lshl_b32 s3, s16, 2
	s_and_b32 s33, s17, 32
	v_lshlrev_b32_e32 v3, 5, v3
	v_ashrrev_i16_sdwa v1, v4, sext(v1) dst_sel:DWORD dst_unused:UNUSED_PAD src0_sel:DWORD src1_sel:BYTE_0
	v_lshlrev_b32_e32 v4, 1, v2
	v_lshrrev_b32_e32 v6, 2, v2
	v_and_or_b32 v5, v2, s1, v5
	s_and_b32 s65, s65, 0xffff
	s_lshl_b32 s1, s0, 10
	s_and_b32 s3, s3, 24
	s_or_b32 s2, s33, s2
	s_bfe_u32 s33, s16, 0x30003
	v_and_b32_e32 v3, 32, v3
	v_bfe_i32 v1, v1, 0, 16
	v_and_b32_e32 v4, 24, v4
	v_and_b32_e32 v6, 4, v6
	s_mov_b32 s67, 0x20000
	s_mov_b32 s66, -1
	v_readlane_b32 s36, v254, 5
	s_or_b32 s88, s3, s33
	s_mov_b64 s[20:21], s[64:65]
	s_add_i32 s33, s1, 0
	v_or3_b32 v4, v5, v6, v4
	v_add_lshl_u32 v1, v3, v1, 1
	v_readlane_b32 s46, v254, 15
	v_readlane_b32 s47, v254, 16
	s_mov_b64 s[22:23], s[66:67]
	s_mov_b64 s[24:25], s[68:69]
	s_mov_b64 s[26:27], s[70:71]
	s_mov_b64 s[28:29], s[72:73]
	s_mov_b64 s[30:31], s[74:75]
	s_lshr_b32 s69, s2, 3
	s_add_i32 s34, s33, 0x10000
	v_lshl_add_u32 v197, v4, 10, v1
	s_and_b32 s9, s47, 0xffff
	s_mov_b32 s8, s46
	s_mov_b32 s10, s66
	s_mov_b32 s11, s67
	s_lshl_b32 s92, s69, 18
	s_mov_b32 m0, s34
	s_add_i32 s35, s33, 0x12000
	v_readlane_b32 s44, v254, 13
	buffer_load_dwordx4 v197, s[8:11], s92 offen lds
	s_or_b32 s1, s92, 0x10000
	s_mov_b32 m0, s35
	v_lshl_add_u32 v196, v2, 10, v1
	v_readlane_b32 s45, v254, 14
	s_lshl_b32 s91, s88, 18
	buffer_load_dwordx4 v197, s[8:11], s1 offen lds
	s_mov_b32 m0, s33
	s_add_i32 s44, s33, 0x2000
	buffer_load_dwordx4 v196, s[20:23], s91 offen lds
	s_or_b32 s1, s91, 0x10000
	s_mov_b32 m0, s44
	s_add_i32 s45, s33, 0x14000
	buffer_load_dwordx4 v196, s[20:23], s1 offen lds
	s_or_b32 s1, s92, 0x20000
	s_mov_b32 m0, s45
	s_add_i32 s46, s33, 0x16000
	v_readlane_b32 s48, v254, 17
	buffer_load_dwordx4 v197, s[8:11], s1 offen lds
	s_or_b32 s1, s92, 0x30000
	s_mov_b32 m0, s46
	s_add_i32 s47, s33, 0x4000
	buffer_load_dwordx4 v197, s[8:11], s1 offen lds
	s_or_b32 s1, s91, 0x20000
	s_mov_b32 m0, s47
	s_add_i32 s48, s33, 0x6000
	buffer_load_dwordx4 v196, s[20:23], s1 offen lds
	s_or_b32 s1, s91, 0x30000
	s_mov_b32 m0, s48
	s_mov_b32 s17, 0
	buffer_load_dwordx4 v196, s[20:23], s1 offen lds
	v_readlane_b32 s37, v254, 6
	v_readlane_b32 s38, v254, 7
	v_readlane_b32 s39, v254, 8
	v_readlane_b32 s40, v254, 9
	v_readlane_b32 s41, v254, 10
	v_readlane_b32 s42, v254, 11
	v_readlane_b32 s43, v254, 12
	v_readlane_b32 s49, v254, 18
	v_readlane_b32 s50, v254, 19
	v_readlane_b32 s51, v254, 20
	s_mov_b64 s[82:83], s[30:31]
	s_ashr_i32 s1, s13, 8
	v_writelane_b32 v254, s16, 3
	s_mov_b64 s[80:81], s[28:29]
	s_mov_b64 s[78:79], s[26:27]
	s_mov_b64 s[76:77], s[24:25]
	s_mov_b64 s[74:75], s[22:23]
	s_mov_b64 s[72:73], s[20:21]
	s_mov_b64 s[70:71], s[62:63]
	s_cmp_lg_u32 s1, 1
	v_writelane_b32 v254, s17, 4
	s_cbranch_scc1 .LBB0_901
	s_barrier

; __device__ __forceinline__ unsigned xb_ld(unsigned* p)              { return __hip_atomic_load(p, __ATOMIC_RELAXED, __HIP_MEMORY_SCOPE_AGENT); }
; __device__ __forceinline__ unsigned xb_add(unsigned* p, unsigned v) { return __hip_atomic_fetch_add(p, v, __ATOMIC_RELAXED, __HIP_MEMORY_SCOPE_AGENT); }
; #define XB_SPIN(cond, bar) do { unsigned _sp = 0; while (cond) { __builtin_amdgcn_s_sleep(1); \
;     if ((++_sp & 255u) == 0u) { if (xb_ld(&(bar)[XB_TMO])) break; if (_sp > XB_SPIN_CAP) { atomicAdd(&(bar)[XB_TMO], 1u); break; } } } } while (0)
; __device__ __forceinline__ void xcd_barrier(const XcdBarrier& b, const int wave) {
;     asm volatile("s_waitcnt vmcnt(0)" ::: "memory");
;     __syncthreads();
;     if (phase_tid(wave) == 0) {
;         unsigned* bar = b.bar;
;         __builtin_amdgcn_s_waitcnt(0);
;         unsigned nloc = b.st[0], nx = b.st[1];
;         if (nloc == 0u) { xcd_barrier_complete(bar, b.x, nloc, nx); b.st[0] = nloc; b.st[1] = nx; }
;         const unsigned old = xb_add(&bar[XB_XSUB(b.x)], 1u);
;         const unsigned gen = old / nloc;
;         if (old + 1u == (gen + 1u) * nloc) {
;             __builtin_amdgcn_fence(__ATOMIC_RELEASE, "agent");
;             asm volatile("s_waitcnt vmcnt(0)" ::: "memory");
;             const unsigned og = xb_add(&bar[XB_TOP], 1u);
;             const unsigned tg = og / nx;
;             if (og + 1u == (tg + 1u) * nx) xb_add(&bar[XB_TOPGEN], 1u);
;             else XB_SPIN(xb_ld(&bar[XB_TOPGEN]) == tg, bar);
;             __builtin_amdgcn_fence(__ATOMIC_ACQUIRE, "agent");
;             xb_add(&bar[XB_XGEN(b.x)], 1u);
;             asm volatile("s_waitcnt vmcnt(0)" ::: "memory");
;         } else {
;             XB_SPIN(xb_ld(&bar[XB_XGEN(b.x)]) == gen, bar);
;             __builtin_amdgcn_fence(__ATOMIC_ACQUIRE, "agent");
;             asm volatile("s_waitcnt vmcnt(0)" ::: "memory");
;         }
;     }
;     __syncthreads();
; }
.LBB0_912:
	s_waitcnt vmcnt(0)
	v_readlane_b32 s0, v255, 25
	s_barrier
	v_mbcnt_lo_u32_b32 v0, -1, 0
	v_mbcnt_hi_u32_b32 v0, -1, v0
	s_nop 0
	v_cmp_eq_u32_e32 vcc, s0, v0
	s_and_saveexec_b64 s[0:1], vcc
	s_cbranch_execz .LBB0_964
	v_readlane_b32 s30, v254, 36
	v_readlane_b32 s31, v254, 37
	v_readlane_b32 s2, v254, 21
	s_add_u32 s10, s30, 0x1400
	s_addc_u32 s11, s31, 0
	s_and_b32 s2, s2, 7
	s_lshl_b32 s16, s2, 8
	s_lshl_b32 s17, s2, 2
	v_mov_b32_e32 v0, s16
	v_mov_b32_e32 v1, 1
	s_waitcnt vmcnt(0) lgkmcnt(0)
	global_atomic_add v1, v0, v1, s[10:11] sc0
	s_waitcnt vmcnt(0)
	v_readfirstlane_b32 s2, v1
	s_add_u32 s2, s2, 1
	s_cmp_lg_u32 s2, 0xe0
	s_cbranch_scc1 .Lmy_gb7_wait
	buffer_wbl2 sc1
	v_mov_b32_e32 v0, s17
	v_mov_b32_e32 v1, 7
	s_waitcnt vmcnt(0)
	global_store_dword v0, v1, s[30:31] sc1

; __device__ __forceinline__ unsigned xb_ld(unsigned* p)              { return __hip_atomic_load(p, __ATOMIC_RELAXED, __HIP_MEMORY_SCOPE_AGENT); }
; __device__ __forceinline__ unsigned xb_add(unsigned* p, unsigned v) { return __hip_atomic_fetch_add(p, v, __ATOMIC_RELAXED, __HIP_MEMORY_SCOPE_AGENT); }
; #define XB_SPIN(cond, bar) do { unsigned _sp = 0; while (cond) { __builtin_amdgcn_s_sleep(1); \
;     if ((++_sp & 255u) == 0u) { if (xb_ld(&(bar)[XB_TMO])) break; if (_sp > XB_SPIN_CAP) { atomicAdd(&(bar)[XB_TMO], 1u); break; } } } } while (0)
; __device__ __forceinline__ void xcd_barrier(const XcdBarrier& b, const int wave) {
;     asm volatile("s_waitcnt vmcnt(0)" ::: "memory");
;     __syncthreads();
;     if (phase_tid(wave) == 0) {
;         unsigned* bar = b.bar;
;         __builtin_amdgcn_s_waitcnt(0);
;         unsigned nloc = b.st[0], nx = b.st[1];
;         if (nloc == 0u) { xcd_barrier_complete(bar, b.x, nloc, nx); b.st[0] = nloc; b.st[1] = nx; }
;         const unsigned old = xb_add(&bar[XB_XSUB(b.x)], 1u);
;         const unsigned gen = old / nloc;
;         if (old + 1u == (gen + 1u) * nloc) {
;             __builtin_amdgcn_fence(__ATOMIC_RELEASE, "agent");
;             asm volatile("s_waitcnt vmcnt(0)" ::: "memory");
;             const unsigned og = xb_add(&bar[XB_TOP], 1u);
;             const unsigned tg = og / nx;
;             if (og + 1u == (tg + 1u) * nx) xb_add(&bar[XB_TOPGEN], 1u);
;             else XB_SPIN(xb_ld(&bar[XB_TOPGEN]) == tg, bar);
;             __builtin_amdgcn_fence(__ATOMIC_ACQUIRE, "agent");
;             xb_add(&bar[XB_XGEN(b.x)], 1u);
;             asm volatile("s_waitcnt vmcnt(0)" ::: "memory");
;         } else {
;             XB_SPIN(xb_ld(&bar[XB_XGEN(b.x)]) == gen, bar);
;             __builtin_amdgcn_fence(__ATOMIC_ACQUIRE, "agent");
;             asm volatile("s_waitcnt vmcnt(0)" ::: "memory");
;         }
;     }
;     __syncthreads();
; }
.Lmy_gb7_poll:
	global_load_dwordx4 v[2:5], v0, s[30:31] sc1
	global_load_dwordx4 v[6:9], v0, s[30:31] offset:16 sc1
	s_waitcnt vmcnt(0)
	v_min_u32_e32 v2, v2, v3
	v_min_u32_e32 v4, v4, v5
	v_min_u32_e32 v6, v6, v7
	v_min_u32_e32 v8, v8, v9
	v_min_u32_e32 v2, v2, v4
	v_min_u32_e32 v6, v6, v8
	v_min_u32_e32 v1, v2, v6
	v_cmp_gt_u32_e32 vcc, 7, v1
	s_cbranch_vccz .Lmy_gb7_done
	s_sleep 1
	s_add_u32 s2, s2, 1
	s_cmp_lt_u32 s2, 0x40000
	s_cbranch_scc1 .Lmy_gb7_poll

; #define PG8_STAGE(bufoff, rs, soff, voff) do { _Pragma("unroll") for (int _i = 0; _i < 2; ++_i) \
;         __builtin_amdgcn_raw_ptr_buffer_load_lds(rs, (LAS void*)(lds + (bufoff) + ldsw + _i * 8192), 16, (voff), (soff) + _i * ((&(voff) == &voffA) ? pieceA : pieceB), 0, 0); } while (0)
; template <class Epi, class Sched, bool FP8 = false>
; __device__ __forceinline__ void gemm_phase(LAS unsigned char* lds, const Gemm g, const Sched& S, const Epi& E, const int wave) {
;     const int tid = phase_tid(wave);
;     const int wid = __builtin_amdgcn_readfirstlane(tid >> 6), lane = tid & 63, wr = wid >> 2, wc = wid & 3, fr = lane & 15, fq = lane >> 4;
;     const int K = g.K, nt = K / BK;
;     unsigned voffA, voffB;
;     {   int R, C; stage_rc(tid * 16, R, C); const int Rb = Epi::PERM ? ((R & ~31) + perm32(R & 31)) : R;
;         voffA = (unsigned)(R * g.lda + C) * 2u; voffB = (unsigned)(Rb * g.ldb + C) * 2u; }
;     const unsigned pieceA = 64u * (unsigned)g.lda * 2u, pieceB = 64u * (unsigned)g.ldb * 2u;
;     const unsigned kstep = (unsigned)(BK * 2);
;     const unsigned hstepA = (unsigned)HALF * g.lda * 2u, hstepB = (unsigned)HALF * g.ldb * 2u;
;     const __amdgpu_buffer_rsrc_t rsA = __builtin_amdgcn_make_buffer_rsrc((void*)g.A, (short)0, -1, 0x00020000), rsB = __builtin_amdgcn_make_buffer_rsrc((void*)g.Bt, (short)0, -1, 0x00020000);
;     const unsigned ldsw = (unsigned)wid * 1024u;
;     const int aoff = lds_byte(wr * 64 + fr, fq * 8), boff = lds_byte(wc * 32 + fr, fq * 8);
;     ...
;     Unit cur, nxt; int ui = 0;
;     if (!S.next(0, cur)) return;
;     f32x4 acc[2][2][4][2];
; #pragma unroll
;     for (int a = 0; a < 2; ++a)
; #pragma unroll
;         for (int b = 0; b < 2; ++b)
; #pragma unroll
;             for (int m = 0; m < 4; ++m)
; #pragma unroll
;                 for (int n = 0; n < 2; ++n) acc[a][b][m][n] = (f32x4){0.f, 0.f, 0.f, 0.f};
;     bf16x8 At[4][2], B0[2][2], B1[2][2];
;     unsigned cA = cur.aoff, cB = cur.boff;
;     PG8_STAGE(PG8_SB(0, 0), rsB, cB, voffB); PG8_STAGE(PG8_SA(0, 0), rsA, cA, voffA); PG8_STAGE(PG8_SB(0, 1), rsB, cB + hstepB, voffB); PG8_STAGE(PG8_SA(0, 1), rsA, cA + hstepA, voffA);
;     if (wr == 1) PG8_BAR;
;     PG8_WAIT_V(4); PG8_BAR;
;     PG8_STAGE(PG8_SB(1, 0), rsB, cB + kstep, voffB); PG8_STAGE(PG8_SA(1, 0), rsA, cA + kstep, voffA); PG8_STAGE(PG8_SB(1, 1), rsB, cB + hstepB + kstep, voffB);
;     PG8_WAIT_V(6); PG8_BAR;
.Lmy_gb7_out:
.LBB0_964:
	s_or_b64 exec, exec, s[0:1]
	s_waitcnt lgkmcnt(0)
	s_barrier
	v_mbcnt_lo_u32_b32 v0, -1, 0
	v_mbcnt_hi_u32_b32 v0, -1, v0
	s_mov_b64 s[82:83], s[74:75]
	v_add_u32_e32 v1, s91, v0
	s_andn2_b64 vcc, exec, s[6:7]
	v_readfirstlane_b32 s3, v1
	s_mov_b64 s[80:81], s[72:73]
	s_mov_b64 s[78:79], s[70:71]
	s_mov_b64 s[76:77], s[68:69]
	s_cbranch_vccnz .LBB0_980
	v_ashrrev_i32_e32 v3, 31, v1
	v_lshrrev_b32_e32 v3, 26, v3
	v_lshlrev_b32_e32 v2, 4, v1
	v_add_u32_e32 v3, v1, v3
	v_bfe_i32 v1, v1, 27, 1
	v_lshrrev_b32_e32 v1, 22, v1
	v_add_u32_e32 v1, v2, v1
	v_and_b32_e32 v1, 0xfffffc00, v1
	v_sub_u32_e32 v1, v2, v1
	v_lshrrev_b32_e32 v2, 4, v1
	v_bitop3_b32 v1, v2, v1, 32 bitop3:0x6c
	v_ashrrev_i32_e32 v4, 31, v1
	v_ashrrev_i32_e32 v3, 6, v3
	v_lshrrev_b32_e32 v4, 26, v4
	v_readlane_b32 s16, v254, 3
	v_lshlrev_b32_e32 v2, 3, v3
	v_add_u32_e32 v4, v1, v4
	v_readlane_b32 s17, v254, 4
	v_and_b32_e32 v2, -16, v2
	v_ashrrev_i32_e32 v5, 6, v4
	v_and_b32_e32 v4, 0xc0, v4
	v_readlane_b32 s17, v255, 33
	s_ashr_i32 s0, s3, 6
	v_add_u32_e32 v2, v5, v2
	v_sub_u32_e32 v1, v1, v4
	v_mov_b32_e32 v4, 1
	v_and_b32_e32 v5, 3, v5
	s_mov_b32 s1, 0x1fffe0
	s_lshr_b32 s2, s16, 3
	s_lshl_b32 s13, s16, 2
	s_and_b32 s33, s17, 32
	v_lshlrev_b32_e32 v3, 5, v3
	v_ashrrev_i16_sdwa v1, v4, sext(v1) dst_sel:DWORD dst_unused:UNUSED_PAD src0_sel:DWORD src1_sel:BYTE_0
	v_lshlrev_b32_e32 v4, 1, v2
	v_lshrrev_b32_e32 v6, 2, v2
	v_and_or_b32 v5, v2, s1, v5
	s_lshl_b32 s1, s0, 10
	s_and_b32 s13, s13, 24
	s_or_b32 s2, s33, s2
	s_bfe_u32 s33, s16, 0x30003
	v_and_b32_e32 v3, 32, v3
	v_bfe_i32 v1, v1, 0, 16
	v_and_b32_e32 v4, 24, v4
	v_and_b32_e32 v6, 4, v6
	v_readlane_b32 s36, v254, 5
	s_or_b32 s67, s13, s33
	s_add_i32 s13, s1, 0
	v_or3_b32 v4, v5, v6, v4
	v_add_lshl_u32 v1, v3, v1, 1
	s_mov_b32 s7, 0x20000
	s_mov_b32 s6, -1
	v_readlane_b32 s50, v254, 19
	v_readlane_b32 s51, v254, 20
	s_lshr_b32 s68, s2, 3
	s_add_i32 s33, s13, 0x10000
	v_lshl_add_u32 v165, v4, 11, v1
	s_and_b32 s9, s51, 0xffff
	s_mov_b32 s8, s50
	s_mov_b32 s10, s6
	s_mov_b32 s11, s7
	s_lshl_b32 s72, s68, 19
	s_mov_b32 m0, s33
	s_add_i32 s34, s13, 0x12000
	buffer_load_dwordx4 v165, s[8:11], s72 offen lds
	s_or_b32 s1, s72, 0x20000
	s_mov_b32 m0, s34
	v_lshl_add_u32 v164, v2, 11, v1
	s_and_b32 s5, s5, 0xffff
	v_readlane_b32 s39, v254, 8
	s_lshl_b32 s71, s67, 19
	buffer_load_dwordx4 v165, s[8:11], s1 offen lds
	s_mov_b32 m0, s13
	s_add_i32 s35, s13, 0x2000
	v_readlane_b32 s41, v254, 10
	buffer_load_dwordx4 v164, s[4:7], s71 offen lds
	s_or_b32 s1, s71, 0x20000
	s_mov_b32 m0, s35
	s_add_i32 s39, s13, 0x14000
	v_readlane_b32 s42, v254, 11
	buffer_load_dwordx4 v164, s[4:7], s1 offen lds
	s_or_b32 s1, s72, 0x40000
	s_mov_b32 m0, s39
	s_add_i32 s41, s13, 0x16000
	v_readlane_b32 s43, v254, 12
	buffer_load_dwordx4 v165, s[8:11], s1 offen lds
	s_or_b32 s1, s72, 0x60000
	s_mov_b32 m0, s41
	s_add_i32 s42, s13, 0x4000
	buffer_load_dwordx4 v165, s[8:11], s1 offen lds
	s_or_b32 s1, s71, 0x40000
	s_mov_b32 m0, s42
	s_add_i32 s43, s13, 0x6000
	buffer_load_dwordx4 v164, s[4:7], s1 offen lds
	s_or_b32 s1, s71, 0x60000
	s_mov_b32 m0, s43
	v_readlane_b32 s44, v254, 13
	buffer_load_dwordx4 v164, s[4:7], s1 offen lds
	s_ashr_i32 s1, s3, 8
	s_cmp_lg_u32 s1, 1
	s_mov_b32 s44, 0
	v_readlane_b32 s37, v254, 6
	v_readlane_b32 s38, v254, 7
	v_readlane_b32 s40, v254, 9
	v_readlane_b32 s45, v254, 14
	v_readlane_b32 s46, v254, 15
	v_readlane_b32 s47, v254, 16
	v_readlane_b32 s48, v254, 17
	v_readlane_b32 s49, v254, 18
	s_cbranch_scc1 .LBB0_967
	s_barrier

; __device__ __forceinline__ unsigned xb_ld(unsigned* p)              { return __hip_atomic_load(p, __ATOMIC_RELAXED, __HIP_MEMORY_SCOPE_AGENT); }
; __device__ __forceinline__ unsigned xb_add(unsigned* p, unsigned v) { return __hip_atomic_fetch_add(p, v, __ATOMIC_RELAXED, __HIP_MEMORY_SCOPE_AGENT); }
; #define XB_SPIN(cond, bar) do { unsigned _sp = 0; while (cond) { __builtin_amdgcn_s_sleep(1); \
;     if ((++_sp & 255u) == 0u) { if (xb_ld(&(bar)[XB_TMO])) break; if (_sp > XB_SPIN_CAP) { atomicAdd(&(bar)[XB_TMO], 1u); break; } } } } while (0)
; __device__ __forceinline__ void xcd_barrier(const XcdBarrier& b, const int wave) {
;     asm volatile("s_waitcnt vmcnt(0)" ::: "memory");
;     __syncthreads();
;     if (phase_tid(wave) == 0) {
;         unsigned* bar = b.bar;
;         __builtin_amdgcn_s_waitcnt(0);
;         unsigned nloc = b.st[0], nx = b.st[1];
;         if (nloc == 0u) { xcd_barrier_complete(bar, b.x, nloc, nx); b.st[0] = nloc; b.st[1] = nx; }
;         const unsigned old = xb_add(&bar[XB_XSUB(b.x)], 1u);
;         const unsigned gen = old / nloc;
;         if (old + 1u == (gen + 1u) * nloc) {
;             __builtin_amdgcn_fence(__ATOMIC_RELEASE, "agent");
;             asm volatile("s_waitcnt vmcnt(0)" ::: "memory");
;             const unsigned og = xb_add(&bar[XB_TOP], 1u);
;             const unsigned tg = og / nx;
;             if (og + 1u == (tg + 1u) * nx) xb_add(&bar[XB_TOPGEN], 1u);
;             else XB_SPIN(xb_ld(&bar[XB_TOPGEN]) == tg, bar);
;             __builtin_amdgcn_fence(__ATOMIC_ACQUIRE, "agent");
;             xb_add(&bar[XB_XGEN(b.x)], 1u);
;             asm volatile("s_waitcnt vmcnt(0)" ::: "memory");
;         } else {
;             XB_SPIN(xb_ld(&bar[XB_XGEN(b.x)]) == gen, bar);
;             __builtin_amdgcn_fence(__ATOMIC_ACQUIRE, "agent");
;             asm volatile("s_waitcnt vmcnt(0)" ::: "memory");
;         }
;     }
;     __syncthreads();
; }
.LBB0_980:
	s_waitcnt vmcnt(0)
	v_readlane_b32 s0, v255, 25
	s_barrier
	v_mbcnt_lo_u32_b32 v0, -1, 0
	v_mbcnt_hi_u32_b32 v0, -1, v0
	s_nop 0
	v_cmp_eq_u32_e32 vcc, s0, v0
	s_and_saveexec_b64 s[0:1], vcc
	s_cbranch_execz .LBB0_1032
	v_readlane_b32 s30, v254, 36
	v_readlane_b32 s31, v254, 37
	v_readlane_b32 s2, v254, 21
	s_add_u32 s10, s30, 0x1400
	s_addc_u32 s11, s31, 0
	s_and_b32 s2, s2, 7
	s_lshl_b32 s16, s2, 8
	s_lshl_b32 s17, s2, 2
	v_mov_b32_e32 v0, s16
	v_mov_b32_e32 v1, 1
	s_waitcnt vmcnt(0) lgkmcnt(0)
	global_atomic_add v1, v0, v1, s[10:11] sc0
	s_waitcnt vmcnt(0)
	v_readfirstlane_b32 s2, v1
	s_add_u32 s2, s2, 1
	s_cmp_lg_u32 s2, 0x100
	s_cbranch_scc1 .Lmy_gb8_wait
	buffer_wbl2 sc1
	v_mov_b32_e32 v0, s17
	v_mov_b32_e32 v1, 8
	s_waitcnt vmcnt(0)
	global_store_dword v0, v1, s[30:31] sc1

; __device__ __forceinline__ unsigned xb_ld(unsigned* p)              { return __hip_atomic_load(p, __ATOMIC_RELAXED, __HIP_MEMORY_SCOPE_AGENT); }
; __device__ __forceinline__ unsigned xb_add(unsigned* p, unsigned v) { return __hip_atomic_fetch_add(p, v, __ATOMIC_RELAXED, __HIP_MEMORY_SCOPE_AGENT); }
; #define XB_SPIN(cond, bar) do { unsigned _sp = 0; while (cond) { __builtin_amdgcn_s_sleep(1); \
;     if ((++_sp & 255u) == 0u) { if (xb_ld(&(bar)[XB_TMO])) break; if (_sp > XB_SPIN_CAP) { atomicAdd(&(bar)[XB_TMO], 1u); break; } } } } while (0)
; __device__ __forceinline__ void xcd_barrier(const XcdBarrier& b, const int wave) {
;     asm volatile("s_waitcnt vmcnt(0)" ::: "memory");
;     __syncthreads();
;     if (phase_tid(wave) == 0) {
;         unsigned* bar = b.bar;
;         __builtin_amdgcn_s_waitcnt(0);
;         unsigned nloc = b.st[0], nx = b.st[1];
;         if (nloc == 0u) { xcd_barrier_complete(bar, b.x, nloc, nx); b.st[0] = nloc; b.st[1] = nx; }
;         const unsigned old = xb_add(&bar[XB_XSUB(b.x)], 1u);
;         const unsigned gen = old / nloc;
;         if (old + 1u == (gen + 1u) * nloc) {
;             __builtin_amdgcn_fence(__ATOMIC_RELEASE, "agent");
;             asm volatile("s_waitcnt vmcnt(0)" ::: "memory");
;             const unsigned og = xb_add(&bar[XB_TOP], 1u);
;             const unsigned tg = og / nx;
;             if (og + 1u == (tg + 1u) * nx) xb_add(&bar[XB_TOPGEN], 1u);
;             else XB_SPIN(xb_ld(&bar[XB_TOPGEN]) == tg, bar);
;             __builtin_amdgcn_fence(__ATOMIC_ACQUIRE, "agent");
;             xb_add(&bar[XB_XGEN(b.x)], 1u);
;             asm volatile("s_waitcnt vmcnt(0)" ::: "memory");
;         } else {
;             XB_SPIN(xb_ld(&bar[XB_XGEN(b.x)]) == gen, bar);
;             __builtin_amdgcn_fence(__ATOMIC_ACQUIRE, "agent");
;             asm volatile("s_waitcnt vmcnt(0)" ::: "memory");
;         }
;     }
;     __syncthreads();
; }
.Lmy_gb8_poll:
	global_load_dwordx4 v[2:5], v0, s[30:31] sc1
	global_load_dwordx4 v[6:9], v0, s[30:31] offset:16 sc1
	s_waitcnt vmcnt(0)
	v_min_u32_e32 v2, v2, v3
	v_min_u32_e32 v4, v4, v5
	v_min_u32_e32 v6, v6, v7
	v_min_u32_e32 v8, v8, v9
	v_min_u32_e32 v2, v2, v4
	v_min_u32_e32 v6, v6, v8
	v_min_u32_e32 v1, v2, v6
	v_cmp_gt_u32_e32 vcc, 8, v1
	s_cbranch_vccz .Lmy_gb8_done
	s_sleep 1
	s_add_u32 s2, s2, 1
	s_cmp_lt_u32 s2, 0x40000
	s_cbranch_scc1 .Lmy_gb8_poll

; #define LAS __attribute__((address_space(3)))
; __device__ __forceinline__ void phase8(const Params& p, LAS unsigned char* lds, const int wave) {
;     const int tid = phase_tid(wave);
;     const int bid = blockIdx.x, lane = tid & 63, wv = tid >> 6;
;     constexpr int HP = ND + 4;
;     LAS float* hs = (LAS float*)lds;
;     LAS float* lg = hs + 16 * HP;
;     LAS float* part = lg + 16 * 32;
;     LAS float* topv = part + 4 * 16 * 32;
;     LAS int* topi = (LAS int*)(topv + 64);
;     LAS int* drow = topi + 64;
;     LAS float* lnA = (LAS float*)(drow + 64);
;     LAS float* lnB = lnA + ND;
;     const int b = (bid * 32) >> 11;
;     const float* sh2 = p.mod + (size_t)b * NMOD + 3 * ND; const float* sc2 = p.mod + (size_t)b * NMOD + 4 * ND;
;     {   const int k = tid * 4; const f32x4 g = ld4(p.ln1_g + k), bb = ld4(p.ln1_b + k), sc = ld4(sc2 + k) + 1.0f, sh = ld4(sh2 + k);
;         *(LAS f32x4*)(lnA + k) = g * sc; *(LAS f32x4*)(lnB + k) = bb * sc + sh; }
.Lmy_gb8_out:
.LBB0_1032:
	s_or_b64 exec, exec, s[0:1]
	v_readlane_b32 s36, v254, 5
	s_waitcnt lgkmcnt(0)
	s_barrier
	v_mbcnt_lo_u32_b32 v18, -1, 0
	v_mbcnt_hi_u32_b32 v18, -1, v18
	v_readlane_b32 s40, v254, 9
	v_add_u32_e32 v84, s91, v18
	v_readlane_b32 s41, v254, 10
	s_mov_b64 s[4:5], s[40:41]
	v_readlane_b32 s0, v255, 31
	v_lshlrev_b32_e32 v16, 2, v84
	v_readlane_b32 s16, v254, 56
	s_add_u32 s0, s4, s0
	v_readlane_b32 s1, v255, 32
	v_ashrrev_i32_e32 v17, 31, v16
	v_readlane_b32 s17, v254, 57
	v_readlane_b32 s18, v254, 58
	v_readlane_b32 s19, v254, 59
	v_readlane_b32 s20, v254, 60
	v_readlane_b32 s21, v254, 61
	v_readlane_b32 s22, v254, 62
	v_readlane_b32 s23, v254, 63
	v_readlane_b32 s24, v255, 0
	v_readlane_b32 s25, v255, 1
	s_addc_u32 s1, s5, s1
	v_lshlrev_b64 v[8:9], 2, v[16:17]
	v_readlane_b32 s26, v255, 2
	v_readlane_b32 s27, v255, 3
	v_readlane_b32 s28, v255, 4
	v_readlane_b32 s29, v255, 5
	v_readlane_b32 s30, v255, 6
	v_readlane_b32 s31, v255, 7
	s_mov_b64 s[16:17], s[24:25]
	s_mov_b64 s[18:19], s[26:27]
	v_lshl_add_u64 v[12:13], s[0:1], 0, v[8:9]
	s_mov_b32 s0, 0x8000
	v_lshl_add_u64 v[0:1], s[16:17], 0, v[8:9]
	v_lshl_add_u64 v[4:5], s[18:19], 0, v[8:9]
	v_add_co_u32_e32 v8, vcc, s0, v12
	s_movk_i32 s0, 0x6000
	s_nop 0
	v_addc_co_u32_e32 v9, vcc, 0, v13, vcc
	global_load_dwordx4 v[8:11], v[8:9], off
	v_add_co_u32_e32 v12, vcc, s0, v12
	global_load_dwordx4 v[0:3], v[0:1], off
	s_nop 0
	v_addc_co_u32_e32 v13, vcc, 0, v13, vcc
	global_load_dwordx4 v[4:7], v[4:5], off
	v_and_b32_e32 v85, 31, v18
	global_load_dwordx4 v[12:15], v[12:13], off
	v_cmp_ne_u32_e32 vcc, 0, v85
	v_and_b32_e32 v17, 63, v18
	s_add_i32 s9, 0, 0x22c00
	v_cndmask_b32_e64 v117, 0, 1, vcc
	v_cmp_lt_u32_e32 vcc, 1, v85
	v_lshlrev_b32_e32 v23, 4, v84
	s_add_i32 s10, 0, 0x24c00
	v_cndmask_b32_e64 v118, 0, 1, vcc
	v_cmp_lt_u32_e32 vcc, 2, v85
	v_and_b32_e32 v20, 15, v18
	v_bfe_u32 v24, v18, 4, 2
	v_cndmask_b32_e64 v119, 0, 1, vcc
	v_cmp_lt_u32_e32 vcc, 3, v85
	v_and_b32_e32 v86, 3, v18
	v_lshlrev_b32_e32 v18, 3, v17
	v_cndmask_b32_e64 v120, 0, 1, vcc
	v_cmp_lt_u32_e32 vcc, 4, v85
	v_cmp_eq_u32_e64 s[0:1], 0, v17
	v_lshlrev_b32_e32 v22, 5, v17
	v_cndmask_b32_e64 v121, 0, 1, vcc
	v_cmp_lt_u32_e32 vcc, 5, v85
	v_add_u32_e32 v17, s9, v23
	v_add_u32_e32 v23, s10, v23
	v_cndmask_b32_e64 v122, 0, 1, vcc
	v_cmp_lt_u32_e32 vcc, 6, v85
	v_ashrrev_i32_e32 v21, 6, v84
	v_lshlrev_b32_e32 v87, 1, v21
	v_cndmask_b32_e64 v123, 0, 1, vcc
	v_cmp_lt_u32_e32 vcc, 7, v85
	s_movk_i32 s8, 0x2010
	v_or_b32_e32 v115, 1, v87
	v_cndmask_b32_e64 v124, 0, 1, vcc
	v_cmp_lt_u32_e32 vcc, 8, v85
	v_ashrrev_i32_e32 v25, 7, v84
	v_and_b32_e32 v29, 64, v84
	v_cndmask_b32_e64 v125, 0, 1, vcc
	v_cmp_lt_u32_e32 vcc, 9, v85
	v_lshlrev_b32_e32 v30, 2, v20
	s_mov_b64 s[20:21], s[28:29]
	v_cndmask_b32_e64 v126, 0, 1, vcc
	v_cmp_lt_u32_e32 vcc, 10, v85
	s_add_i32 s11, 0, 0x20900
	v_and_b32_e32 v31, 0x3fffffe0, v84
	v_cndmask_b32_e64 v127, 0, 1, vcc
	v_cmp_lt_u32_e32 vcc, 11, v85
	v_mov_b32_e32 v64, 0
	s_movk_i32 s3, 0x4020
	v_cndmask_b32_e64 v128, 0, 1, vcc
	v_cmp_lt_u32_e32 vcc, 12, v85
	s_add_i32 s13, 0, 0x20100
	s_add_i32 s34, 0, 0x22a00
	v_cndmask_b32_e64 v129, 0, 1, vcc
	v_cmp_lt_u32_e32 vcc, 13, v85
	s_add_i32 s35, 0, 0x22b00
	v_mad_u32_u24 v26, v20, s8, 0
	v_cndmask_b32_e64 v130, 0, 1, vcc
	v_cmp_lt_u32_e32 vcc, 14, v85
	v_lshlrev_b32_e32 v34, 11, v25
	v_add_u32_e32 v35, s11, v29
	v_cndmask_b32_e64 v131, 0, 1, vcc
	v_cmp_lt_u32_e32 vcc, 15, v85
	v_lshlrev_b32_e32 v31, 2, v31
	v_lshlrev_b32_e32 v36, 5, v21
	v_cndmask_b32_e64 v132, 0, 1, vcc
	v_cmp_lt_u32_e32 vcc, 16, v85
	v_add_u32_e32 v98, s9, v22
	v_readlane_b32 s38, v254, 7
	v_cndmask_b32_e64 v133, 0, 1, vcc
	v_cmp_lt_u32_e32 vcc, 17, v85
	v_readlane_b32 s39, v254, 8
	s_mov_b64 s[22:23], s[30:31]
	s_waitcnt vmcnt(3)
; #define LAS __attribute__((address_space(3)))
; __device__ __forceinline__ void phase8(const Params& p, LAS unsigned char* lds, const int wave) {
;     ...
;     {   const int k = tid * 4; const f32x4 g = ld4(p.ln1_g + k), bb = ld4(p.ln1_b + k), sc = ld4(sc2 + k) + 1.0f, sh = ld4(sh2 + k);
;         *(LAS f32x4*)(lnA + k) = g * sc; *(LAS f32x4*)(lnB + k) = bb * sc + sh; }
;     __syncthreads();
;     ...
;             const int r = tid >> 5, e = tid & 31; const LAS float* l = lg + r * 32; const float mine = l[e]; int rank = 0;
; #pragma unroll
;             for (int q = 0; q < 8; ++q) { const f32x4 o = *(const LAS f32x4*)(l + q * 4);
; #pragma unroll
;                 for (int j = 0; j < 4; ++j) rank += (o[j] > mine || (o[j] == mine && (q * 4 + j) < e)) ? 1 : 0; }
;             if (rank < 4) { topv[r * 4 + rank] = mine; topi[r * 4 + rank] = e; } }
;         __syncthreads();
;         if (tid < 64) { const int r = tid >> 2, k = tid & 3, m = mb + r; const f32x4 tv = *(const LAS f32x4*)(topv + r * 4); const int ei = topi[r * 4 + k];
;             const float e0 = 1.0f, e1 = expf(tv[1] - tv[0]), e2 = expf(tv[2] - tv[0]), e3 = expf(tv[3] - tv[0]); const float sum = (e0 + e1) + (e2 + e3);
;             const float mineexp = k == 0 ? e0 : (k == 1 ? e1 : (k == 2 ? e2 : e3));
;             const unsigned rk = atomicAdd(&p.ctl[CW_CNT + 64 * ei], 1u);
;             const int dr = ei * ECAP + (int)rk; drow[r * 4 + k] = dr; p.dest[m * 4 + k] = dr; p.prob[m * 4 + k] = mineexp / sum; }
	v_pk_add_f32 v[10:11], v[10:11], 1.0 op_sel_hi:[1,0]
	v_pk_add_f32 v[8:9], v[8:9], 1.0 op_sel_hi:[1,0]
	v_cndmask_b32_e64 v134, 0, 1, vcc
	s_waitcnt vmcnt(2)
	v_pk_mul_f32 v[2:3], v[2:3], v[10:11]
	v_pk_mul_f32 v[0:1], v[0:1], v[8:9]
	v_cmp_lt_u32_e32 vcc, 18, v85
	v_mov_b32_e32 v19, v64
	s_add_i32 s33, 0, 0x22900
	s_waitcnt vmcnt(0)
	v_pk_fma_f32 v[6:7], v[6:7], v[10:11], v[14:15]
	v_pk_fma_f32 v[4:5], v[4:5], v[8:9], v[12:13]
	ds_write_b128 v17, v[0:3]
	ds_write_b128 v23, v[4:7]
	v_or_b32_e32 v0, 16, v22
	v_add_u32_e32 v101, s9, v0
	v_add_u32_e32 v102, s10, v0
	v_or_b32_e32 v0, 0x800, v22
	v_add_u32_e32 v103, s9, v0
	v_add_u32_e32 v104, s10, v0
	v_or_b32_e32 v0, 0x810, v22
	v_cndmask_b32_e64 v135, 0, 1, vcc
	v_cmp_lt_u32_e32 vcc, 19, v85
	v_add_u32_e32 v105, s9, v0
	v_add_u32_e32 v106, s10, v0
	v_or_b32_e32 v0, 0x1000, v22
	v_cndmask_b32_e64 v136, 0, 1, vcc
	v_cmp_lt_u32_e32 vcc, 20, v85
	v_add_u32_e32 v107, s9, v0
	v_add_u32_e32 v108, s10, v0
	v_or_b32_e32 v0, 0x1010, v22
	v_cndmask_b32_e64 v137, 0, 1, vcc
	v_cmp_lt_u32_e32 vcc, 21, v85
	v_add_u32_e32 v109, s9, v0
	v_add_u32_e32 v110, s10, v0
	v_or_b32_e32 v0, 0x1800, v22
	v_cndmask_b32_e64 v138, 0, 1, vcc
	v_cmp_lt_u32_e32 vcc, 22, v85
	v_add_u32_e32 v111, s9, v0
	v_add_u32_e32 v112, s10, v0
	v_or_b32_e32 v0, 0x1810, v22
	v_cndmask_b32_e64 v139, 0, 1, vcc
	v_cmp_lt_u32_e32 vcc, 23, v85
	v_add_u32_e32 v113, s9, v0
	v_add_u32_e32 v114, s10, v0
	v_mul_lo_u32 v0, v115, s8
	v_cndmask_b32_e64 v140, 0, 1, vcc
	v_cmp_lt_u32_e32 vcc, 24, v85
	v_add3_u32 v116, 0, v0, v22
	v_lshl_or_b32 v0, v25, 9, v24
	v_cndmask_b32_e64 v141, 0, 1, vcc
	v_cmp_lt_u32_e32 vcc, 25, v85
	v_ashrrev_i32_e32 v1, 31, v0
	v_lshlrev_b64 v[0:1], 7, v[0:1]
	v_cndmask_b32_e64 v142, 0, 1, vcc
	v_cmp_lt_u32_e32 vcc, 26, v85
	v_or3_b32 v0, v0, v29, v30
	v_lshl_add_u64 v[0:1], s[20:21], 0, v[0:1]
	v_cndmask_b32_e64 v143, 0, 1, vcc
	v_cmp_lt_u32_e32 vcc, 27, v85
	s_mov_b64 s[8:9], 0x3e00
	v_lshlrev_b32_e32 v27, 2, v24
	v_cndmask_b32_e64 v144, 0, 1, vcc
	v_cmp_lt_u32_e32 vcc, 28, v85
	v_lshlrev_b32_e32 v28, 9, v24
	v_lshlrev_b32_e32 v20, 2, v85
	v_cndmask_b32_e64 v145, 0, 1, vcc
	v_cmp_lt_u32_e32 vcc, 29, v85
	v_ashrrev_i32_e32 v32, 3, v84
	v_and_b32_e32 v33, 0x3ffffffc, v84
	v_add_u32_e32 v88, s11, v16
	v_add_u32_e32 v89, s13, v16
	v_add_u32_e32 v92, s34, v16
	v_add_u32_e32 v93, s35, v16
	v_mul_lo_u32 v16, v21, s3
	v_add_u32_e32 v96, s13, v31
	v_add3_u32 v2, v35, v30, v34
	v_cndmask_b32_e64 v146, 0, 1, vcc
	v_cmp_eq_u32_e32 vcc, 31, v85
	v_mov_b32_e32 v23, v64
	v_mov_b32_e32 v21, v64
	v_lshl_add_u64 v[72:73], v[0:1], 0, s[8:9]
	v_add_u32_e32 v0, 0, v36
	s_mov_b32 s2, 0
	v_cmp_gt_i32_e64 s[4:5], 64, v84
	v_cmp_eq_u32_e64 s[6:7], 2, v86
	v_and_b32_e32 v90, -4, v32
	v_lshl_add_u32 v91, v33, 2, s33
	v_add3_u32 v94, v26, v34, v27
	v_add3_u32 v95, s11, v31, v20
	v_add_u32_e32 v97, v96, v20
	v_add_u32_e32 v99, s10, v22
	v_add3_u32 v100, 0, v16, v22
	s_movk_i32 s3, 0x1000
	v_cndmask_b32_e64 v147, 0, 1, vcc
	v_lshl_add_u64 v[66:67], s[68:69], 0, v[22:23]
	v_lshl_add_u64 v[68:69], s[22:23], 0, v[20:21]
	v_lshl_add_u64 v[70:71], s[84:85], 0, v[18:19]
	s_mov_b64 s[40:41], -1
	s_mov_b64 s[8:9], 0x1000
	s_mov_b64 s[10:11], 0x1800
	v_mov_b32_e32 v148, 0x3727c5ac
	s_mov_b32 s13, 0x800000
	s_mov_b64 s[38:39], 0x4000
	v_add_u32_e32 v149, v2, v28
	s_mov_b32 s33, 0x3fb8aa3b
	s_mov_b32 s34, 0xc2ce8ed0
	s_mov_b32 s35, 0x42b17218
	v_mov_b32_e32 v150, 1
	v_add_u32_e32 v151, 0x22b00, v0
	v_mov_b32_e32 v152, 0x7f800000
	v_readlane_b32 s37, v254, 6
	v_readlane_b32 s42, v254, 11
	v_readlane_b32 s43, v254, 12
	v_readlane_b32 s44, v254, 13
	v_readlane_b32 s45, v254, 14
	v_readlane_b32 s46, v254, 15
	v_readlane_b32 s47, v254, 16
	v_readlane_b32 s48, v254, 17
	v_readlane_b32 s49, v254, 18
	v_readlane_b32 s50, v254, 19
	v_readlane_b32 s51, v254, 20
	s_waitcnt lgkmcnt(0)
	s_barrier
	s_branch .LBB0_1036

; __device__ __forceinline__ unsigned xb_ld(unsigned* p)              { return __hip_atomic_load(p, __ATOMIC_RELAXED, __HIP_MEMORY_SCOPE_AGENT); }
; __device__ __forceinline__ unsigned xb_add(unsigned* p, unsigned v) { return __hip_atomic_fetch_add(p, v, __ATOMIC_RELAXED, __HIP_MEMORY_SCOPE_AGENT); }
; #define XB_SPIN(cond, bar) do { unsigned _sp = 0; while (cond) { __builtin_amdgcn_s_sleep(1); \
;     if ((++_sp & 255u) == 0u) { if (xb_ld(&(bar)[XB_TMO])) break; if (_sp > XB_SPIN_CAP) { atomicAdd(&(bar)[XB_TMO], 1u); break; } } } } while (0)
; __device__ __forceinline__ void xcd_barrier(const XcdBarrier& b, const int wave) {
;     asm volatile("s_waitcnt vmcnt(0)" ::: "memory");
;     __syncthreads();
;     if (phase_tid(wave) == 0) {
;         unsigned* bar = b.bar;
;         __builtin_amdgcn_s_waitcnt(0);
;         unsigned nloc = b.st[0], nx = b.st[1];
;         if (nloc == 0u) { xcd_barrier_complete(bar, b.x, nloc, nx); b.st[0] = nloc; b.st[1] = nx; }
;         const unsigned old = xb_add(&bar[XB_XSUB(b.x)], 1u);
;         const unsigned gen = old / nloc;
;         if (old + 1u == (gen + 1u) * nloc) {
;             __builtin_amdgcn_fence(__ATOMIC_RELEASE, "agent");
;             asm volatile("s_waitcnt vmcnt(0)" ::: "memory");
;             const unsigned og = xb_add(&bar[XB_TOP], 1u);
;             const unsigned tg = og / nx;
;             if (og + 1u == (tg + 1u) * nx) xb_add(&bar[XB_TOPGEN], 1u);
;             else XB_SPIN(xb_ld(&bar[XB_TOPGEN]) == tg, bar);
;             __builtin_amdgcn_fence(__ATOMIC_ACQUIRE, "agent");
;             xb_add(&bar[XB_XGEN(b.x)], 1u);
;             asm volatile("s_waitcnt vmcnt(0)" ::: "memory");
.LBB0_1174:
	s_barrier
	s_waitcnt vmcnt(0)
	v_readlane_b32 s0, v255, 25
	s_barrier
	v_mbcnt_lo_u32_b32 v0, -1, 0
	v_mbcnt_hi_u32_b32 v0, -1, v0
	s_nop 0
	v_cmp_eq_u32_e32 vcc, s0, v0
	s_and_saveexec_b64 s[0:1], vcc
	s_cbranch_execz .LBB0_1226
	v_readlane_b32 s30, v254, 36
	v_readlane_b32 s31, v254, 37
	v_readlane_b32 s2, v254, 21
	s_add_u32 s10, s30, 0x1400
	s_addc_u32 s11, s31, 0
	s_and_b32 s2, s2, 7
	s_lshl_b32 s16, s2, 8
	s_lshl_b32 s17, s2, 2
	v_mov_b32_e32 v0, s16
	v_mov_b32_e32 v1, 1
	s_waitcnt vmcnt(0) lgkmcnt(0)
	global_atomic_add v1, v0, v1, s[10:11] sc0
	s_waitcnt vmcnt(0)
	v_readfirstlane_b32 s2, v1
	s_add_u32 s2, s2, 1
	s_cmp_lg_u32 s2, 0x120
	s_cbranch_scc1 .Lmy_gb9_wait
	buffer_wbl2 sc1
	v_mov_b32_e32 v0, s17
	v_mov_b32_e32 v1, 9
	s_waitcnt vmcnt(0)
	global_store_dword v0, v1, s[30:31] sc1

; __device__ __forceinline__ unsigned xb_ld(unsigned* p)              { return __hip_atomic_load(p, __ATOMIC_RELAXED, __HIP_MEMORY_SCOPE_AGENT); }
; __device__ __forceinline__ unsigned xb_add(unsigned* p, unsigned v) { return __hip_atomic_fetch_add(p, v, __ATOMIC_RELAXED, __HIP_MEMORY_SCOPE_AGENT); }
; #define XB_SPIN(cond, bar) do { unsigned _sp = 0; while (cond) { __builtin_amdgcn_s_sleep(1); \
;     if ((++_sp & 255u) == 0u) { if (xb_ld(&(bar)[XB_TMO])) break; if (_sp > XB_SPIN_CAP) { atomicAdd(&(bar)[XB_TMO], 1u); break; } } } } while (0)
; __device__ __forceinline__ void xcd_barrier(const XcdBarrier& b, const int wave) {
;     ...
;             else XB_SPIN(xb_ld(&bar[XB_TOPGEN]) == tg, bar);
;             __builtin_amdgcn_fence(__ATOMIC_ACQUIRE, "agent");
;             xb_add(&bar[XB_XGEN(b.x)], 1u);
;             asm volatile("s_waitcnt vmcnt(0)" ::: "memory");
;         } else {
;             XB_SPIN(xb_ld(&bar[XB_XGEN(b.x)]) == gen, bar);
.Lmy_gb9_poll:
	global_load_dwordx4 v[2:5], v0, s[30:31] sc1
	global_load_dwordx4 v[6:9], v0, s[30:31] offset:16 sc1
	s_waitcnt vmcnt(0)
	v_min_u32_e32 v2, v2, v3
	v_min_u32_e32 v4, v4, v5
	v_min_u32_e32 v6, v6, v7
	v_min_u32_e32 v8, v8, v9
	v_min_u32_e32 v2, v2, v4
	v_min_u32_e32 v6, v6, v8
	v_min_u32_e32 v1, v2, v6
	v_cmp_gt_u32_e32 vcc, 9, v1
	s_cbranch_vccz .Lmy_gb9_done
	s_sleep 1
	s_add_u32 s2, s2, 1
	s_cmp_lt_u32 s2, 0x40000
	s_cbranch_scc1 .Lmy_gb9_poll

; #define LAS __attribute__((address_space(3)))
; __device__ __forceinline__ unsigned xb_ld(unsigned* p)              { return __hip_atomic_load(p, __ATOMIC_RELAXED, __HIP_MEMORY_SCOPE_AGENT); }
; __global__ void __launch_bounds__(NTHREADS, 2) fwd(Params p) {
;     ...
;         const int t_ = phase_tid(wave); LAS unsigned* tab = (LAS unsigned*)(lds + LDS_MISC); LAS int* cnt = (LAS int*)(lds + LDS_MISC + 1280);
;         if (t_ < NE) cnt[t_] = ((int)xb_ld(&p.ctl[CW_CNT + 64 * t_]) + 255) >> 8;
;         __syncthreads();
.Lmy_gb9_out:
.LBB0_1226:
	s_or_b64 exec, exec, s[0:1]
	s_waitcnt lgkmcnt(0)
	s_barrier
	v_mbcnt_lo_u32_b32 v16, -1, 0
	v_mbcnt_hi_u32_b32 v16, -1, v16
	s_nop 0
	v_add_u32_e32 v0, s91, v16
	v_cmp_gt_i32_e32 vcc, 32, v0
	s_and_saveexec_b64 s[0:1], vcc
	s_cbranch_execz .LBB0_1228
	v_lshlrev_b32_e32 v2, 6, v0
	v_readlane_b32 s36, v254, 5
	v_ashrrev_i32_e32 v3, 31, v2
	v_readlane_b32 s37, v254, 6
	v_readlane_b32 s38, v254, 7
	v_readlane_b32 s39, v254, 8
	v_lshl_add_u64 v[2:3], v[2:3], 2, s[36:37]
	global_load_dword v1, v[2:3], off sc1
	v_lshl_add_u32 v2, v0, 2, 0
	v_add_u32_e32 v2, 0x20500, v2
	v_readlane_b32 s40, v254, 9
	v_readlane_b32 s41, v254, 10
	v_readlane_b32 s42, v254, 11
	v_readlane_b32 s43, v254, 12
	v_readlane_b32 s44, v254, 13
	v_readlane_b32 s45, v254, 14
	v_readlane_b32 s46, v254, 15
	v_readlane_b32 s47, v254, 16
	v_readlane_b32 s48, v254, 17
	v_readlane_b32 s49, v254, 18
	v_readlane_b32 s50, v254, 19
	v_readlane_b32 s51, v254, 20
	s_waitcnt vmcnt(0)
	v_add_u32_e32 v1, 0xff, v1
	v_ashrrev_i32_e32 v1, 8, v1
	ds_write_b32 v2, v1

; __device__ __forceinline__ unsigned xb_ld(unsigned* p)              { return __hip_atomic_load(p, __ATOMIC_RELAXED, __HIP_MEMORY_SCOPE_AGENT); }
; __device__ __forceinline__ unsigned xb_add(unsigned* p, unsigned v) { return __hip_atomic_fetch_add(p, v, __ATOMIC_RELAXED, __HIP_MEMORY_SCOPE_AGENT); }
; #define XB_SPIN(cond, bar) do { unsigned _sp = 0; while (cond) { __builtin_amdgcn_s_sleep(1); \
;     if ((++_sp & 255u) == 0u) { if (xb_ld(&(bar)[XB_TMO])) break; if (_sp > XB_SPIN_CAP) { atomicAdd(&(bar)[XB_TMO], 1u); break; } } } } while (0)
; __device__ __forceinline__ void xcd_barrier(const XcdBarrier& b, const int wave) {
;     asm volatile("s_waitcnt vmcnt(0)" ::: "memory");
;     __syncthreads();
;     if (phase_tid(wave) == 0) {
;         unsigned* bar = b.bar;
;         __builtin_amdgcn_s_waitcnt(0);
;         unsigned nloc = b.st[0], nx = b.st[1];
;         if (nloc == 0u) { xcd_barrier_complete(bar, b.x, nloc, nx); b.st[0] = nloc; b.st[1] = nx; }
;         const unsigned old = xb_add(&bar[XB_XSUB(b.x)], 1u);
;         const unsigned gen = old / nloc;
;         if (old + 1u == (gen + 1u) * nloc) {
;             __builtin_amdgcn_fence(__ATOMIC_RELEASE, "agent");
;             asm volatile("s_waitcnt vmcnt(0)" ::: "memory");
;             const unsigned og = xb_add(&bar[XB_TOP], 1u);
;             const unsigned tg = og / nx;
;             if (og + 1u == (tg + 1u) * nx) xb_add(&bar[XB_TOPGEN], 1u);
;             else XB_SPIN(xb_ld(&bar[XB_TOPGEN]) == tg, bar);
;             __builtin_amdgcn_fence(__ATOMIC_ACQUIRE, "agent");
;             xb_add(&bar[XB_XGEN(b.x)], 1u);
;             asm volatile("s_waitcnt vmcnt(0)" ::: "memory");
.LBB0_1290:
	s_waitcnt vmcnt(0)
	v_readlane_b32 s0, v255, 25
	s_barrier
	v_mbcnt_lo_u32_b32 v0, -1, 0
	v_mbcnt_hi_u32_b32 v0, -1, v0
	s_nop 0
	v_cmp_eq_u32_e32 vcc, s0, v0
	s_and_saveexec_b64 s[0:1], vcc
	s_cbranch_execz .LBB0_1342
	v_readlane_b32 s30, v254, 36
	v_readlane_b32 s31, v254, 37
	v_readlane_b32 s2, v254, 21
	s_add_u32 s10, s30, 0x1400
	s_addc_u32 s11, s31, 0
	s_and_b32 s2, s2, 7
	s_lshl_b32 s16, s2, 8
	s_lshl_b32 s17, s2, 2
	v_mov_b32_e32 v0, s16
	v_mov_b32_e32 v1, 1
	s_waitcnt vmcnt(0) lgkmcnt(0)
	global_atomic_add v1, v0, v1, s[10:11] sc0
	s_waitcnt vmcnt(0)
	v_readfirstlane_b32 s2, v1
	s_add_u32 s2, s2, 1
	s_cmp_lg_u32 s2, 0x140
	s_cbranch_scc1 .Lmy_gb10_wait
	buffer_wbl2 sc1
	v_mov_b32_e32 v0, s17
	v_mov_b32_e32 v1, 10
	s_waitcnt vmcnt(0)
	global_store_dword v0, v1, s[30:31] sc1

; __device__ __forceinline__ unsigned xb_ld(unsigned* p)              { return __hip_atomic_load(p, __ATOMIC_RELAXED, __HIP_MEMORY_SCOPE_AGENT); }
; __device__ __forceinline__ unsigned xb_add(unsigned* p, unsigned v) { return __hip_atomic_fetch_add(p, v, __ATOMIC_RELAXED, __HIP_MEMORY_SCOPE_AGENT); }
; #define XB_SPIN(cond, bar) do { unsigned _sp = 0; while (cond) { __builtin_amdgcn_s_sleep(1); \
;     if ((++_sp & 255u) == 0u) { if (xb_ld(&(bar)[XB_TMO])) break; if (_sp > XB_SPIN_CAP) { atomicAdd(&(bar)[XB_TMO], 1u); break; } } } } while (0)
; __device__ __forceinline__ void xcd_barrier(const XcdBarrier& b, const int wave) {
;     ...
;             else XB_SPIN(xb_ld(&bar[XB_TOPGEN]) == tg, bar);
;             __builtin_amdgcn_fence(__ATOMIC_ACQUIRE, "agent");
;             xb_add(&bar[XB_XGEN(b.x)], 1u);
;             asm volatile("s_waitcnt vmcnt(0)" ::: "memory");
;         } else {
;             XB_SPIN(xb_ld(&bar[XB_XGEN(b.x)]) == gen, bar);
.Lmy_gb10_poll:
	global_load_dwordx4 v[2:5], v0, s[30:31] sc1
	global_load_dwordx4 v[6:9], v0, s[30:31] offset:16 sc1
	s_waitcnt vmcnt(0)
	v_min_u32_e32 v2, v2, v3
	v_min_u32_e32 v4, v4, v5
	v_min_u32_e32 v6, v6, v7
	v_min_u32_e32 v8, v8, v9
	v_min_u32_e32 v2, v2, v4
	v_min_u32_e32 v6, v6, v8
	v_min_u32_e32 v1, v2, v6
	v_cmp_gt_u32_e32 vcc, 10, v1
	s_cbranch_vccz .Lmy_gb10_done
	s_sleep 1
	s_add_u32 s2, s2, 1
	s_cmp_lt_u32 s2, 0x40000
	s_cbranch_scc1 .Lmy_gb10_poll

; #define PG8_BAR __builtin_amdgcn_s_barrier()
; template <class Epi, class Sched, bool FP8 = false>
; __device__ __forceinline__ void gemm_phase(LAS unsigned char* lds, const Gemm g, const Sched& S, const Epi& E, const int wave) {
;     const int tid = phase_tid(wave);
;     const int wid = __builtin_amdgcn_readfirstlane(tid >> 6), lane = tid & 63, wr = wid >> 2, wc = wid & 3, fr = lane & 15, fq = lane >> 4;
;     const int K = g.K, nt = K / BK;
;     unsigned voffA, voffB;
;     {   int R, C; stage_rc(tid * 16, R, C); const int Rb = Epi::PERM ? ((R & ~31) + perm32(R & 31)) : R;
;         voffA = (unsigned)(R * g.lda + C) * 2u; voffB = (unsigned)(Rb * g.ldb + C) * 2u; }
;     const unsigned pieceA = 64u * (unsigned)g.lda * 2u, pieceB = 64u * (unsigned)g.ldb * 2u;
;     const unsigned kstep = (unsigned)(BK * 2);
;     const unsigned hstepA = (unsigned)HALF * g.lda * 2u, hstepB = (unsigned)HALF * g.ldb * 2u;
;     const __amdgpu_buffer_rsrc_t rsA = __builtin_amdgcn_make_buffer_rsrc((void*)g.A, (short)0, -1, 0x00020000), rsB = __builtin_amdgcn_make_buffer_rsrc((void*)g.Bt, (short)0, -1, 0x00020000);
;     const unsigned ldsw = (unsigned)wid * 1024u;
;     const int aoff = lds_byte(wr * 64 + fr, fq * 8), boff = lds_byte(wc * 32 + fr, fq * 8);
;     ...
;     Unit cur, nxt; int ui = 0;
;     if (!S.next(0, cur)) return;
;     f32x4 acc[2][2][4][2];
; #pragma unroll
;     for (int a = 0; a < 2; ++a)
; #pragma unroll
;         for (int b = 0; b < 2; ++b)
; #pragma unroll
;             for (int m = 0; m < 4; ++m)
; #pragma unroll
;                 for (int n = 0; n < 2; ++n) acc[a][b][m][n] = (f32x4){0.f, 0.f, 0.f, 0.f};
;     bf16x8 At[4][2], B0[2][2], B1[2][2];
;     unsigned cA = cur.aoff, cB = cur.boff;
;     PG8_STAGE(PG8_SB(0, 0), rsB, cB, voffB); PG8_STAGE(PG8_SA(0, 0), rsA, cA, voffA); PG8_STAGE(PG8_SB(0, 1), rsB, cB + hstepB, voffB); PG8_STAGE(PG8_SA(0, 1), rsA, cA + hstepA, voffA);
;     if (wr == 1) PG8_BAR;
;     PG8_WAIT_V(4); PG8_BAR;
;     PG8_STAGE(PG8_SB(1, 0), rsB, cB + kstep, voffB); PG8_STAGE(PG8_SA(1, 0), rsA, cA + kstep, voffA); PG8_STAGE(PG8_SB(1, 1), rsB, cB + hstepB + kstep, voffB);
;     __device__ bool next(int i, Unit& u) const {
;         const int L = i * (G - ncv) + (c - ncv); if (c < ncv || L >= ntiles * nN) return false;
;         u.pm = __builtin_amdgcn_readfirstlane((int)tile_e[L / nN]); u.pn = L % nN; u.e = u.pm >> 5;
.Lmy_gb10_out:
.LBB0_1342:
	s_or_b64 exec, exec, s[0:1]
	s_waitcnt lgkmcnt(0)
	s_barrier
	v_mbcnt_lo_u32_b32 v0, -1, 0
	v_mbcnt_hi_u32_b32 v0, -1, v0
	s_cmp_lt_i32 s86, 0
	v_add_u32_e32 v1, s91, v0
	s_nop 0
	v_readfirstlane_b32 s1, v1
	s_cbranch_scc1 .LBB0_1355
	s_lshl_b32 s3, s3, 3
	s_cmp_ge_i32 s86, s3
	s_cbranch_scc1 .LBB0_1355
	v_ashrrev_i32_e32 v3, 31, v1
	v_lshrrev_b32_e32 v3, 26, v3
	v_lshlrev_b32_e32 v2, 4, v1
	v_add_u32_e32 v3, v1, v3
	v_bfe_i32 v1, v1, 27, 1
	v_lshrrev_b32_e32 v1, 22, v1
	v_add_u32_e32 v1, v2, v1
	v_and_b32_e32 v1, 0xfffffc00, v1
	v_sub_u32_e32 v1, v2, v1
	v_lshrrev_b32_e32 v2, 4, v1
	v_bitop3_b32 v1, v2, v1, 32 bitop3:0x6c
	v_ashrrev_i32_e32 v4, 31, v1
	v_ashrrev_i32_e32 v3, 6, v3
	v_lshrrev_b32_e32 v4, 26, v4
	v_lshlrev_b32_e32 v2, 3, v3
	v_add_u32_e32 v4, v1, v4
	v_and_b32_e32 v2, -16, v2
	v_ashrrev_i32_e32 v5, 6, v4
	v_add_u32_e32 v2, v5, v2
	v_and_b32_e32 v4, 0xc0, v4
	v_and_b32_e32 v5, 3, v5
	s_mov_b32 s2, 0x1fffe0
	v_sub_u32_e32 v1, v1, v4
	v_mov_b32_e32 v4, 1
	v_and_or_b32 v5, v2, s2, v5
	s_lshr_b32 s2, s86, 1
	v_lshlrev_b32_e32 v3, 5, v3
	v_ashrrev_i16_sdwa v1, v4, sext(v1) dst_sel:DWORD dst_unused:UNUSED_PAD src0_sel:DWORD src1_sel:BYTE_0
	v_lshlrev_b32_e32 v4, 1, v2
	v_lshrrev_b32_e32 v6, 2, v2
	s_and_b32 s2, s2, 0x7ffffffc
	v_and_b32_e32 v3, 32, v3
	v_bfe_i32 v1, v1, 0, 16
	v_and_b32_e32 v4, 24, v4
	v_and_b32_e32 v6, 4, v6
	s_add_i32 s2, s2, 0
	v_or3_b32 v4, v5, v6, v4
	v_add_lshl_u32 v1, v3, v1, 1
	s_add_i32 s2, s2, 0x20000
	v_lshl_add_u32 v136, v2, 11, v1
	v_lshl_add_u32 v137, v4, 11, v1
	v_mov_b32_e32 v1, s2
	ds_read_b32 v1, v1
	s_ashr_i32 s0, s1, 6
	s_lshl_b32 s8, s0, 10
	s_and_b32 s12, s86, 7
	s_add_i32 s14, s8, 0
	s_waitcnt lgkmcnt(0)
	v_readfirstlane_b32 s50, v1
	s_ashr_i32 s10, s50, 5
	s_mov_b32 s7, 0x20000
	s_mov_b32 s6, -1
	s_lshl_b32 s9, s10, 22
	s_lshl_b32 s11, s12, 19
	s_add_i32 s15, s14, 0x10000
	s_and_b32 s57, s57, 0xffff
	s_mov_b32 s58, s6
	s_mov_b32 s59, s7
	s_or_b32 s52, s9, s11
	s_mov_b32 m0, s15
	s_add_i32 s16, s14, 0x12000
	buffer_load_dwordx4 v137, s[56:59], s52 offen lds
	s_or_b32 s8, s52, 0x20000
	s_mov_b32 m0, s16
	s_and_b32 s5, s5, 0xffff
	s_lshl_b32 s2, s50, 19
	buffer_load_dwordx4 v137, s[56:59], s8 offen lds
	s_mov_b32 m0, s14
	s_add_i32 s17, s14, 0x2000
	buffer_load_dwordx4 v136, s[4:7], s2 offen lds
	s_or_b32 s8, s2, 0x20000
	s_mov_b32 m0, s17
	s_add_i32 s18, s14, 0x14000
	buffer_load_dwordx4 v136, s[4:7], s8 offen lds
	s_or_b32 s8, s52, 0x40000
	s_mov_b32 m0, s18
	s_add_i32 s19, s14, 0x16000
	buffer_load_dwordx4 v137, s[56:59], s8 offen lds
	s_or_b32 s8, s52, 0x60000
	s_mov_b32 m0, s19
	s_add_i32 s20, s14, 0x4000
	buffer_load_dwordx4 v137, s[56:59], s8 offen lds
	s_or_b32 s8, s2, 0x40000
	s_mov_b32 m0, s20
	s_add_i32 s21, s14, 0x6000
	buffer_load_dwordx4 v136, s[4:7], s8 offen lds
	s_or_b32 s8, s2, 0x60000
	s_mov_b32 m0, s21
	s_mov_b32 s33, 0
	buffer_load_dwordx4 v136, s[4:7], s8 offen lds
	s_ashr_i32 s8, s1, 8
	s_cmp_lg_u32 s8, 1
	s_cbranch_scc1 .LBB0_1346
	s_barrier

; __device__ __forceinline__ unsigned xb_ld(unsigned* p)              { return __hip_atomic_load(p, __ATOMIC_RELAXED, __HIP_MEMORY_SCOPE_AGENT); }
; __device__ __forceinline__ unsigned xb_add(unsigned* p, unsigned v) { return __hip_atomic_fetch_add(p, v, __ATOMIC_RELAXED, __HIP_MEMORY_SCOPE_AGENT); }
; #define XB_SPIN(cond, bar) do { unsigned _sp = 0; while (cond) { __builtin_amdgcn_s_sleep(1); \
;     if ((++_sp & 255u) == 0u) { if (xb_ld(&(bar)[XB_TMO])) break; if (_sp > XB_SPIN_CAP) { atomicAdd(&(bar)[XB_TMO], 1u); break; } } } } while (0)
; __device__ __forceinline__ void xcd_barrier(const XcdBarrier& b, const int wave) {
;     asm volatile("s_waitcnt vmcnt(0)" ::: "memory");
;     __syncthreads();
;     if (phase_tid(wave) == 0) {
;         unsigned* bar = b.bar;
;         __builtin_amdgcn_s_waitcnt(0);
;         unsigned nloc = b.st[0], nx = b.st[1];
;         if (nloc == 0u) { xcd_barrier_complete(bar, b.x, nloc, nx); b.st[0] = nloc; b.st[1] = nx; }
;         const unsigned old = xb_add(&bar[XB_XSUB(b.x)], 1u);
;         const unsigned gen = old / nloc;
;         if (old + 1u == (gen + 1u) * nloc) {
;             __builtin_amdgcn_fence(__ATOMIC_RELEASE, "agent");
;             asm volatile("s_waitcnt vmcnt(0)" ::: "memory");
;             const unsigned og = xb_add(&bar[XB_TOP], 1u);
;             const unsigned tg = og / nx;
;             if (og + 1u == (tg + 1u) * nx) xb_add(&bar[XB_TOPGEN], 1u);
;             else XB_SPIN(xb_ld(&bar[XB_TOPGEN]) == tg, bar);
;             __builtin_amdgcn_fence(__ATOMIC_ACQUIRE, "agent");
;             xb_add(&bar[XB_XGEN(b.x)], 1u);
;             asm volatile("s_waitcnt vmcnt(0)" ::: "memory");
.LBB0_1355:
	s_waitcnt vmcnt(0)
	v_readlane_b32 s0, v255, 25
	s_barrier
	v_mbcnt_lo_u32_b32 v0, -1, 0
	v_mbcnt_hi_u32_b32 v0, -1, v0
	s_nop 0
	v_cmp_eq_u32_e32 vcc, s0, v0
	s_and_saveexec_b64 s[0:1], vcc
	v_readlane_b32 s16, v254, 22
	v_readlane_b32 s24, v254, 30
	v_readlane_b32 s25, v254, 31
	v_readlane_b32 s26, v254, 32
	v_readlane_b32 s27, v254, 33
	v_readlane_b32 s30, v254, 36
	v_readlane_b32 s31, v254, 37
	v_readlane_b32 s17, v254, 23
	v_readlane_b32 s18, v254, 24
	v_readlane_b32 s19, v254, 25
	v_readlane_b32 s20, v254, 26
	v_readlane_b32 s21, v254, 27
	v_readlane_b32 s22, v254, 28
	v_readlane_b32 s23, v254, 29
	v_readlane_b32 s28, v254, 34
	v_readlane_b32 s29, v254, 35
	s_cbranch_execz .LBB0_1407
	v_readlane_b32 s30, v254, 36
	v_readlane_b32 s31, v254, 37
	v_readlane_b32 s2, v254, 21
	s_add_u32 s10, s30, 0x1400
	s_addc_u32 s11, s31, 0
	s_and_b32 s2, s2, 7
	s_lshl_b32 s16, s2, 8
	s_lshl_b32 s17, s2, 2
	v_mov_b32_e32 v0, s16
	v_mov_b32_e32 v1, 1
	s_waitcnt vmcnt(0) lgkmcnt(0)
	global_atomic_add v1, v0, v1, s[10:11] sc0
	s_waitcnt vmcnt(0)
	v_readfirstlane_b32 s2, v1
	s_add_u32 s2, s2, 1
	s_cmp_lg_u32 s2, 0x160
	s_cbranch_scc1 .Lmy_gb11_wait
	buffer_wbl2 sc1
	v_mov_b32_e32 v0, s17
	v_mov_b32_e32 v1, 11
	s_waitcnt vmcnt(0)
	global_store_dword v0, v1, s[30:31] sc1

; __device__ __forceinline__ unsigned xb_ld(unsigned* p)              { return __hip_atomic_load(p, __ATOMIC_RELAXED, __HIP_MEMORY_SCOPE_AGENT); }
; __device__ __forceinline__ unsigned xb_add(unsigned* p, unsigned v) { return __hip_atomic_fetch_add(p, v, __ATOMIC_RELAXED, __HIP_MEMORY_SCOPE_AGENT); }
; #define XB_SPIN(cond, bar) do { unsigned _sp = 0; while (cond) { __builtin_amdgcn_s_sleep(1); \
;     if ((++_sp & 255u) == 0u) { if (xb_ld(&(bar)[XB_TMO])) break; if (_sp > XB_SPIN_CAP) { atomicAdd(&(bar)[XB_TMO], 1u); break; } } } } while (0)
; __device__ __forceinline__ void xcd_barrier(const XcdBarrier& b, const int wave) {
;     ...
;             else XB_SPIN(xb_ld(&bar[XB_TOPGEN]) == tg, bar);
;             __builtin_amdgcn_fence(__ATOMIC_ACQUIRE, "agent");
;             xb_add(&bar[XB_XGEN(b.x)], 1u);
;             asm volatile("s_waitcnt vmcnt(0)" ::: "memory");
;         } else {
;             XB_SPIN(xb_ld(&bar[XB_XGEN(b.x)]) == gen, bar);
.Lmy_gb11_poll:
	global_load_dwordx4 v[2:5], v0, s[30:31] sc1
	global_load_dwordx4 v[6:9], v0, s[30:31] offset:16 sc1
	s_waitcnt vmcnt(0)
	v_min_u32_e32 v2, v2, v3
	v_min_u32_e32 v4, v4, v5
	v_min_u32_e32 v6, v6, v7
	v_min_u32_e32 v8, v8, v9
	v_min_u32_e32 v2, v2, v4
	v_min_u32_e32 v6, v6, v8
	v_min_u32_e32 v1, v2, v6
	v_cmp_gt_u32_e32 vcc, 11, v1
	s_cbranch_vccz .Lmy_gb11_done
	s_sleep 1
	s_add_u32 s2, s2, 1
	s_cmp_lt_u32 s2, 0x40000
	s_cbranch_scc1 .Lmy_gb11_poll

; #define LAS __attribute__((address_space(3)))
; __device__ __forceinline__ f32x4 ld4nt(const float* p) { return __builtin_nontemporal_load((const f32x4*)p); }
; __device__ __forceinline__ u32x4 ldu4nt(const void* p) { return __builtin_nontemporal_load((const u32x4*)p); }
; __device__ __forceinline__ void phase13(const Params& p, LAS unsigned char* lds, const int wave) {
;     const int tid = phase_tid(wave);
;     const int bid = blockIdx.x, lane0 = tid & 63, wv = wave;
;     const int GW = gridDim.x * NWAVES;
;     LAS float* L2G = (LAS float*)lds; LAS float* L2B = L2G + ND;
;     {   const int k = tid * 4; *(LAS f32x4*)(L2G + k) = ld4(p.ln2_g + k); *(LAS f32x4*)(L2B + k) = ld4(p.ln2_b + k); }
;     __syncthreads();
;     for (int m = bid * NWAVES + wv; m < NM; m += GW) { const int b = m >> 11;
;         int lane = lane0; asm volatile("" : "+v"(lane));
;         const float* g2 = p.mod + (size_t)b * NMOD + 5 * ND;
;         int d[4]; float pr[4]; const f32x2 st = *(const f32x2*)(p.lnst + (size_t)m * 2);
; #pragma unroll
;         for (int k = 0; k < 4; ++k) { d[k] = p.dest[m * 4 + k]; pr[k] = p.prob[m * 4 + k]; }
;         f32x4 z[8]; float s = 0.f; u32x4 yq[4][4];
; #pragma unroll
;         for (int j = 0; j < 4; ++j) {
; #pragma unroll
;             for (int k = 0; k < 4; ++k) yq[j][k] = ldu4nt(p.yb + (size_t)d[k] * ND + j * 512 + lane * 8);
;             z[2 * j] = ld4nt(p.z1 + (size_t)m * ND + j * 512 + lane * 8); z[2 * j + 1] = ld4nt(p.z1 + (size_t)m * ND + j * 512 + lane * 8 + 4); }
.Lmy_gb11_out:
.LBB0_1407:
	s_or_b64 exec, exec, s[0:1]
	s_lshl_b32 s0, s87, 8
	s_waitcnt lgkmcnt(0)
	s_barrier
	v_mbcnt_lo_u32_b32 v0, -1, 0
	v_mbcnt_hi_u32_b32 v0, -1, v0
	s_nop 0
	v_lshl_add_u32 v10, v0, 2, s0
	v_ashrrev_i32_e32 v11, 31, v10
	v_lshlrev_b64 v[6:7], 2, v[10:11]
	v_lshl_add_u64 v[2:3], s[24:25], 0, v[6:7]
	global_load_dwordx4 v[2:5], v[2:3], off
	v_lshl_add_u64 v[6:7], s[26:27], 0, v[6:7]
	global_load_dwordx4 v[6:9], v[6:7], off
	v_readlane_b32 s0, v255, 8
	s_add_i32 s0, s87, s0
	s_cmpk_gt_i32 s0, 0x1fff
	v_lshl_add_u32 v1, v10, 2, 0
	s_waitcnt vmcnt(1)
	ds_write_b128 v1, v[2:5]
	s_waitcnt vmcnt(0)
	ds_write_b128 v1, v[6:9] offset:8192
	s_waitcnt lgkmcnt(0)
	s_barrier
	s_cbranch_scc1 .LBB0_1410
	v_readlane_b32 s36, v254, 5
	v_readlane_b32 s44, v254, 13
	v_readlane_b32 s45, v254, 14
	v_readlane_b32 s46, v254, 15
	v_readlane_b32 s47, v254, 16
	v_readlane_b32 s48, v254, 17
	v_readlane_b32 s49, v254, 18
	v_readlane_b32 s50, v254, 19
	v_readlane_b32 s51, v254, 20
	v_readlane_b32 s44, v254, 22
	s_lshl_b32 s1, s87, 2
	v_readlane_b32 s2, v255, 33
	v_readlane_b32 s45, v254, 23
	v_readlane_b32 s46, v254, 24
	v_readlane_b32 s47, v254, 25
	v_readlane_b32 s48, v254, 26
	v_readlane_b32 s49, v254, 27
	v_readlane_b32 s50, v254, 28
	v_readlane_b32 s51, v254, 29
	v_readlane_b32 s52, v254, 30
	v_readlane_b32 s53, v254, 31
	v_readlane_b32 s54, v254, 32
	v_readlane_b32 s55, v254, 33
	v_readlane_b32 s56, v254, 34
	v_readlane_b32 s57, v254, 35
	v_readlane_b32 s58, v254, 36
	v_readlane_b32 s59, v254, 37
	s_add_i32 s2, s2, s1
	s_ashr_i32 s1, s0, 31
	s_ashr_i32 s91, s90, 31
	s_mov_b64 s[28:29], s[56:57]
	v_readlane_b32 s44, v254, 56
	s_lshl_b32 s19, s89, 5
	s_lshl_b64 s[4:5], s[0:1], 13
	s_lshl_b64 s[6:7], s[90:91], 13
	s_lshl_b64 s[8:9], s[0:1], 3
	v_readlane_b32 s45, v254, 57
	v_readlane_b32 s46, v254, 58
	v_readlane_b32 s47, v254, 59
	v_readlane_b32 s52, v255, 0
	v_readlane_b32 s53, v255, 1
	s_add_u32 s8, s62, s8
	v_readlane_b32 s54, v255, 2
	v_readlane_b32 s55, v255, 3
	s_mov_b64 s[44:45], s[52:53]
	v_and_b32_e32 v54, 63, v0
	s_addc_u32 s9, s63, s9
	s_lshl_b64 s[10:11], s[90:91], 3
	v_mov_b32_e32 v40, 0
	s_mov_b64 s[12:13], 0x1000
	s_movk_i32 s1, 0x1000
	s_mov_b64 s[14:15], 0x1800
	s_mov_b64 s[16:17], 0xa000
	s_mov_b32 s18, 0x3f9837f0
	s_mov_b64 s[20:21], 0xb000
	s_mov_b32 s26, 0xb000
	s_mov_b64 s[22:23], 0xb800
	v_mov_b32_e32 v55, 0x3727c5ac
	s_mov_b32 s27, 0x800000
	v_readlane_b32 s40, v254, 9
	v_readlane_b32 s41, v254, 10
	s_mov_b64 s[46:47], s[54:55]
	v_readlane_b32 s37, v254, 6
	v_readlane_b32 s38, v254, 7
	v_readlane_b32 s39, v254, 8
	v_readlane_b32 s42, v254, 11
	v_readlane_b32 s43, v254, 12
	v_readlane_b32 s48, v254, 60
	v_readlane_b32 s49, v254, 61
	v_readlane_b32 s50, v254, 62
	v_readlane_b32 s51, v254, 63
	v_readlane_b32 s56, v255, 4
	v_readlane_b32 s57, v255, 5
	v_readlane_b32 s58, v255, 6
	v_readlane_b32 s59, v255, 7
